# combo17 + K-loop handoffs trimmed: hipcc's per-segment s_setprio flips and the already-satisfied lgkmcnt(0) between the barrier release and the first MFMA deleted (all four GEMMs)
# baseline (speedup 1.0000x reference)
.LBB0_243:
	s_add_u32 s22, s22, 0x20080
	s_addc_u32 s23, s23, 0
	s_add_u32 s17, s24, 0x100
	v_mov_b32_e32 v183, 0x1200
	s_addc_u32 s19, s25, 0
	s_mov_b32 s28, -2
	ds_read_b128 v[138:141], v134
	ds_read_b128 v[146:149], v134 offset:2048
	ds_read_b128 v[142:145], v135
	ds_read_b128 v[150:153], v135 offset:2048
	ds_read_b128 v[154:157], v134 offset:16384
	ds_read_b128 v[162:165], v134 offset:18432
	ds_read_b128 v[158:161], v135 offset:16384
	ds_read_b128 v[166:169], v135 offset:18432
	s_add_u32 s24, s22, 0xfffe0080
	s_addc_u32 s25, s23, -1
	s_cmp_eq_u32 s28, 4
	s_cselect_b32 s25, s5, s25
	s_cselect_b32 s24, s4, s24
	s_cselect_b32 s27, s21, s19
	s_cselect_b32 s26, s20, s17
	v_mov_b32_e32 v128, v136
	ds_read_b128 v[170:173], v132
	ds_read_b128 v[194:197], v132 offset:2048
	ds_read_b128 v[174:177], v133
	ds_read_b128 v[198:201], v133 offset:2048
	ds_read_b128 v[228:231], v132 offset:4096
	ds_read_b128 v[236:239], v132 offset:6144
	ds_read_b128 v[232:235], v133 offset:4096
	ds_read_b128 v[240:243], v133 offset:6144
	s_add_i32 m0, s30, 0xc000
	s_nop 0
	global_load_lds_dwordx4 v128, s[22:23]
	v_mov_b32_e32 v128, v137
	s_add_i32 m0, s30, 0xe000
	s_nop 0
	global_load_lds_dwordx4 v128, s[22:23]
	s_waitcnt vmcnt(8)
	s_waitcnt lgkmcnt(0)
	s_barrier
	v_mfma_f32_16x16x128_f8f6f4 v[124:127], v[138:145], v[170:177], 0
	v_mfma_f32_16x16x128_f8f6f4 v[120:123], v[146:153], v[170:177], 0
	v_mfma_f32_16x16x128_f8f6f4 v[108:111], v[138:145], v[194:201], 0
	v_mfma_f32_16x16x128_f8f6f4 v[104:107], v[146:153], v[194:201], 0
	v_mfma_f32_16x16x128_f8f6f4 v[128:131], v[138:145], v[228:235], 0
	v_mfma_f32_16x16x128_f8f6f4 v[178:181], v[146:153], v[228:235], 0
	v_mfma_f32_16x16x128_f8f6f4 v[202:205], v[138:145], v[236:243], 0
	v_mfma_f32_16x16x128_f8f6f4 v[244:247], v[146:153], v[236:243], 0
	v_mfma_f32_16x16x128_f8f6f4 v[116:119], v[154:161], v[170:177], 0
	v_mfma_f32_16x16x128_f8f6f4 v[112:115], v[162:169], v[170:177], 0
	v_mfma_f32_16x16x128_f8f6f4 v[100:103], v[154:161], v[194:201], 0
	v_mfma_f32_16x16x128_f8f6f4 v[96:99], v[162:169], v[194:201], 0
	v_mfma_f32_16x16x128_f8f6f4 v[170:173], v[154:161], v[228:235], 0
	v_mfma_f32_16x16x128_f8f6f4 v[174:177], v[162:169], v[228:235], 0
	v_mfma_f32_16x16x128_f8f6f4 v[194:197], v[154:161], v[236:243], 0
	v_mfma_f32_16x16x128_f8f6f4 v[198:201], v[162:169], v[236:243], 0
	s_barrier
	v_mov_b32_e32 v182, v136
	s_mov_b32 m0, s31
	s_nop 2
	ds_read_b128 v[64:67], v132 offset:16384
	ds_read_b128 v[72:75], v132 offset:18432
	ds_read_b128 v[68:71], v133 offset:16384
	ds_read_b128 v[76:79], v133 offset:18432
	ds_read_b128 v[80:83], v132 offset:20480
	ds_read_b128 v[88:91], v132 offset:22528
	ds_read_b128 v[84:87], v133 offset:20480
	ds_read_b128 v[92:95], v133 offset:22528
	s_add_u32 s64, s26, 0x20000
	global_load_lds_dwordx4 v182, s[26:27]
	v_mov_b32_e32 v182, v137
	s_mov_b32 m0, s33
	s_addc_u32 s65, s27, 0
	global_load_lds_dwordx4 v182, s[26:27]
	v_mov_b32_e32 v182, v136
	s_mov_b32 m0, s34
	s_nop 0
	global_load_lds_dwordx4 v182, s[64:65]
	v_mov_b32_e32 v182, v137
	s_mov_b32 m0, s35
	s_nop 0
	global_load_lds_dwordx4 v182, s[64:65]
	v_mov_b32_e32 v182, v136
	s_mov_b32 m0, s30
	s_nop 0
	global_load_lds_dwordx4 v182, s[24:25]
	v_mov_b32_e32 v182, v137
	s_mov_b32 m0, s36
	s_nop 0
	global_load_lds_dwordx4 v182, s[24:25]
	s_waitcnt vmcnt(8)
	s_waitcnt lgkmcnt(0)
	s_barrier
	v_mfma_f32_16x16x128_f8f6f4 v[60:63], v[138:145], v[64:71], 0
	v_mfma_f32_16x16x128_f8f6f4 v[56:59], v[146:153], v[64:71], 0
	v_mfma_f32_16x16x128_f8f6f4 v[228:231], v[138:145], v[72:79], 0
	v_mfma_f32_16x16x128_f8f6f4 v[232:235], v[146:153], v[72:79], 0
	v_mfma_f32_16x16x128_f8f6f4 v[236:239], v[138:145], v[80:87], 0
	v_mfma_f32_16x16x128_f8f6f4 v[240:243], v[146:153], v[80:87], 0
	v_mfma_f32_16x16x128_f8f6f4 v[248:251], v[138:145], v[88:95], 0
	v_mfma_f32_16x16x128_f8f6f4 v[186:189], v[146:153], v[88:95], 0
	v_mfma_f32_16x16x128_f8f6f4 v[52:55], v[154:161], v[64:71], 0
	v_mfma_f32_16x16x128_f8f6f4 v[48:51], v[162:169], v[64:71], 0
	v_mfma_f32_16x16x128_f8f6f4 v[190:193], v[154:161], v[72:79], 0
	v_mfma_f32_16x16x128_f8f6f4 v[210:213], v[162:169], v[72:79], 0
	v_mfma_f32_16x16x128_f8f6f4 v[206:209], v[154:161], v[80:87], 0
	v_mfma_f32_16x16x128_f8f6f4 v[214:217], v[162:169], v[80:87], 0
	v_mfma_f32_16x16x128_f8f6f4 v[222:225], v[154:161], v[88:95], 0
	v_mfma_f32_16x16x128_f8f6f4 v[218:221], v[162:169], v[88:95], 0
	s_barrier
	s_nop 4
	ds_read_b128 v[0:3], v134 offset:32768
	ds_read_b128 v[16:19], v134 offset:34816
	ds_read_b128 v[4:7], v135 offset:32768
	ds_read_b128 v[20:23], v135 offset:34816
	ds_read_b128 v[138:141], v134 offset:49152
	ds_read_b128 v[146:149], v134 offset:51200
	ds_read_b128 v[142:145], v135 offset:49152
	ds_read_b128 v[150:153], v135 offset:51200
	s_add_u32 s64, s24, 0x20000
	v_mov_b32_e32 v64, v136
	s_mov_b32 m0, s37
	ds_read_b128 v[8:11], v132 offset:32768
	ds_read_b128 v[24:27], v132 offset:34816
	ds_read_b128 v[12:15], v133 offset:32768
	ds_read_b128 v[28:31], v133 offset:34816
	ds_read_b128 v[32:35], v132 offset:36864
	ds_read_b128 v[40:43], v132 offset:38912
	ds_read_b128 v[36:39], v133 offset:36864
	ds_read_b128 v[44:47], v133 offset:38912
	s_addc_u32 s65, s25, 0
	s_nop 0
	global_load_lds_dwordx4 v64, s[64:65]
	v_mov_b32_e32 v64, v137
	s_mov_b32 m0, s38
	s_nop 0
	global_load_lds_dwordx4 v64, s[64:65]
	s_waitcnt vmcnt(8)
	s_waitcnt lgkmcnt(0)
	s_barrier
	v_mfma_f32_16x16x128_f8f6f4 v[124:127], v[0:7], v[8:15], v[124:127]
	v_mfma_f32_16x16x128_f8f6f4 v[120:123], v[16:23], v[8:15], v[120:123]
	v_mfma_f32_16x16x128_f8f6f4 v[108:111], v[0:7], v[24:31], v[108:111]
	v_mfma_f32_16x16x128_f8f6f4 v[104:107], v[16:23], v[24:31], v[104:107]
	v_mfma_f32_16x16x128_f8f6f4 v[92:95], v[0:7], v[32:39], v[128:131]
	v_mfma_f32_16x16x128_f8f6f4 v[88:91], v[16:23], v[32:39], v[178:181]
	v_mfma_f32_16x16x128_f8f6f4 v[76:79], v[0:7], v[40:47], v[202:205]
	v_mfma_f32_16x16x128_f8f6f4 v[72:75], v[16:23], v[40:47], v[244:247]
	v_mfma_f32_16x16x128_f8f6f4 v[116:119], v[138:145], v[8:15], v[116:119]
	v_mfma_f32_16x16x128_f8f6f4 v[112:115], v[146:153], v[8:15], v[112:115]
	v_mfma_f32_16x16x128_f8f6f4 v[100:103], v[138:145], v[24:31], v[100:103]
	v_mfma_f32_16x16x128_f8f6f4 v[96:99], v[146:153], v[24:31], v[96:99]
	v_mfma_f32_16x16x128_f8f6f4 v[84:87], v[138:145], v[32:39], v[170:173]
	v_mfma_f32_16x16x128_f8f6f4 v[80:83], v[146:153], v[32:39], v[174:177]
	v_mfma_f32_16x16x128_f8f6f4 v[68:71], v[138:145], v[40:47], v[194:197]
	v_mfma_f32_16x16x128_f8f6f4 v[64:67], v[146:153], v[40:47], v[198:201]
	s_barrier
	v_mov_b32_e32 v184, v136
	ds_read_b128 v[32:35], v132 offset:49152
	ds_read_b128 v[154:157], v132 offset:51200
	ds_read_b128 v[36:39], v133 offset:49152
	ds_read_b128 v[158:161], v133 offset:51200
	ds_read_b128 v[162:165], v132 offset:53248
	ds_read_b128 v[170:173], v132 offset:55296
	ds_read_b128 v[166:169], v133 offset:53248
	ds_read_b128 v[174:177], v133 offset:55296
	s_mov_b32 m0, s42
	v_lshl_add_u64 v[8:9], s[26:27], 0, v[184:185]
	v_lshl_add_u64 v[8:9], v[8:9], 0, s[46:47]
	v_mov_b32_e32 v184, v137
	global_load_lds_dwordx4 v[8:9], off
	s_mov_b32 m0, s43
	v_lshl_add_u64 v[8:9], s[26:27], 0, v[184:185]
	v_lshl_add_u64 v[8:9], v[8:9], 0, s[46:47]
	global_load_lds_dwordx4 v[8:9], off
	s_add_u32 s26, s26, 0x20080
	v_mov_b32_e32 v8, v136
	s_addc_u32 s27, s27, 0
	s_mov_b32 m0, s50
	v_mov_b32_e32 v184, v136
	global_load_lds_dwordx4 v8, s[26:27]
	v_mov_b32_e32 v8, v137
	s_mov_b32 m0, s51
	s_nop 0
	global_load_lds_dwordx4 v8, s[26:27]
	s_mov_b32 m0, s44
	v_lshl_add_u64 v[8:9], s[24:25], 0, v[184:185]
	v_lshl_add_u64 v[8:9], v[8:9], 0, s[46:47]
	v_mov_b32_e32 v184, v137
	global_load_lds_dwordx4 v[8:9], off
	s_mov_b32 m0, s49
	v_lshl_add_u64 v[8:9], s[24:25], 0, v[184:185]
	v_lshl_add_u64 v[8:9], v[8:9], 0, s[46:47]
	global_load_lds_dwordx4 v[8:9], off
	s_waitcnt vmcnt(8)
	s_waitcnt lgkmcnt(0)
	s_barrier
	v_mfma_f32_16x16x128_f8f6f4 v[60:63], v[0:7], v[32:39], v[60:63]
	v_mfma_f32_16x16x128_f8f6f4 v[56:59], v[16:23], v[32:39], v[56:59]
	v_mfma_f32_16x16x128_f8f6f4 v[44:47], v[0:7], v[154:161], v[228:231]
	v_mfma_f32_16x16x128_f8f6f4 v[40:43], v[16:23], v[154:161], v[232:235]
	v_mfma_f32_16x16x128_f8f6f4 v[28:31], v[0:7], v[162:169], v[236:239]
	v_mfma_f32_16x16x128_f8f6f4 v[24:27], v[16:23], v[162:169], v[240:243]
	v_mfma_f32_16x16x128_f8f6f4 v[12:15], v[0:7], v[170:177], v[248:251]
	v_mfma_f32_16x16x128_f8f6f4 v[8:11], v[16:23], v[170:177], v[186:189]
	v_mfma_f32_16x16x128_f8f6f4 v[52:55], v[138:145], v[32:39], v[52:55]
	v_mfma_f32_16x16x128_f8f6f4 v[48:51], v[146:153], v[32:39], v[48:51]
	v_mfma_f32_16x16x128_f8f6f4 v[36:39], v[138:145], v[154:161], v[190:193]
	v_mfma_f32_16x16x128_f8f6f4 v[32:35], v[146:153], v[154:161], v[210:213]
	v_mfma_f32_16x16x128_f8f6f4 v[20:23], v[138:145], v[162:169], v[206:209]
	v_mfma_f32_16x16x128_f8f6f4 v[16:19], v[146:153], v[162:169], v[214:217]
	v_mfma_f32_16x16x128_f8f6f4 v[4:7], v[138:145], v[170:177], v[222:225]
	v_mfma_f32_16x16x128_f8f6f4 v[0:3], v[146:153], v[170:177], v[218:221]
	s_barrier
	s_add_i32 s28, s28, 2
	s_add_u32 s22, s22, 0x100
	s_addc_u32 s23, s23, 0
	s_add_u32 s17, s17, 0x100
	s_addc_u32 s19, s19, 0
.LBB0_244:
	ds_read_b128 v[138:141], v134
	ds_read_b128 v[146:149], v134 offset:2048
	ds_read_b128 v[142:145], v135
	ds_read_b128 v[150:153], v135 offset:2048
	ds_read_b128 v[154:157], v134 offset:16384
	ds_read_b128 v[162:165], v134 offset:18432
	ds_read_b128 v[158:161], v135 offset:16384
	ds_read_b128 v[166:169], v135 offset:18432
	s_add_u32 s24, s22, 0xfffe0080
	s_addc_u32 s25, s23, -1
	s_cmp_eq_u32 s28, 4
	s_cselect_b32 s25, s5, s25
	s_cselect_b32 s24, s4, s24
	s_cselect_b32 s27, s21, s19
	s_cselect_b32 s26, s20, s17
	v_mov_b32_e32 v128, v136
	ds_read_b128 v[170:173], v132
	ds_read_b128 v[194:197], v132 offset:2048
	ds_read_b128 v[174:177], v133
	ds_read_b128 v[198:201], v133 offset:2048
	ds_read_b128 v[228:231], v132 offset:4096
	ds_read_b128 v[236:239], v132 offset:6144
	ds_read_b128 v[232:235], v133 offset:4096
	ds_read_b128 v[240:243], v133 offset:6144
	s_add_i32 m0, s30, 0xc000
	s_nop 0
	global_load_lds_dwordx4 v128, s[22:23]
	v_mov_b32_e32 v128, v137
	s_add_i32 m0, s30, 0xe000
	s_nop 0
	global_load_lds_dwordx4 v128, s[22:23]
	s_waitcnt vmcnt(8)
	s_waitcnt lgkmcnt(0)
	s_barrier
	v_mfma_f32_16x16x128_f8f6f4 v[124:127], v[138:145], v[170:177], v[124:127]
	v_mfma_f32_16x16x128_f8f6f4 v[120:123], v[146:153], v[170:177], v[120:123]
	v_mfma_f32_16x16x128_f8f6f4 v[108:111], v[138:145], v[194:201], v[108:111]
	v_mfma_f32_16x16x128_f8f6f4 v[104:107], v[146:153], v[194:201], v[104:107]
	v_mfma_f32_16x16x128_f8f6f4 v[128:131], v[138:145], v[228:235], v[92:95]
	v_mfma_f32_16x16x128_f8f6f4 v[178:181], v[146:153], v[228:235], v[88:91]
	v_mfma_f32_16x16x128_f8f6f4 v[202:205], v[138:145], v[236:243], v[76:79]
	v_mfma_f32_16x16x128_f8f6f4 v[244:247], v[146:153], v[236:243], v[72:75]
	v_mfma_f32_16x16x128_f8f6f4 v[116:119], v[154:161], v[170:177], v[116:119]
	v_mfma_f32_16x16x128_f8f6f4 v[112:115], v[162:169], v[170:177], v[112:115]
	v_mfma_f32_16x16x128_f8f6f4 v[100:103], v[154:161], v[194:201], v[100:103]
	v_mfma_f32_16x16x128_f8f6f4 v[96:99], v[162:169], v[194:201], v[96:99]
	v_mfma_f32_16x16x128_f8f6f4 v[170:173], v[154:161], v[228:235], v[84:87]
	v_mfma_f32_16x16x128_f8f6f4 v[174:177], v[162:169], v[228:235], v[80:83]
	v_mfma_f32_16x16x128_f8f6f4 v[194:197], v[154:161], v[236:243], v[68:71]
	v_mfma_f32_16x16x128_f8f6f4 v[198:201], v[162:169], v[236:243], v[64:67]
	s_barrier
	v_mov_b32_e32 v182, v136
	s_mov_b32 m0, s31
	s_nop 2
	ds_read_b128 v[64:67], v132 offset:16384
	ds_read_b128 v[72:75], v132 offset:18432
	ds_read_b128 v[68:71], v133 offset:16384
	ds_read_b128 v[76:79], v133 offset:18432
	ds_read_b128 v[80:83], v132 offset:20480
	ds_read_b128 v[88:91], v132 offset:22528
	ds_read_b128 v[84:87], v133 offset:20480
	ds_read_b128 v[92:95], v133 offset:22528
	s_add_u32 s64, s26, 0x20000
	global_load_lds_dwordx4 v182, s[26:27]
	v_mov_b32_e32 v182, v137
	s_mov_b32 m0, s33
	s_addc_u32 s65, s27, 0
	global_load_lds_dwordx4 v182, s[26:27]
	v_mov_b32_e32 v182, v136
	s_mov_b32 m0, s34
	s_nop 0
	global_load_lds_dwordx4 v182, s[64:65]
	v_mov_b32_e32 v182, v137
	s_mov_b32 m0, s35
	s_nop 0
	global_load_lds_dwordx4 v182, s[64:65]
	v_mov_b32_e32 v182, v136
	s_mov_b32 m0, s30
	s_nop 0
	global_load_lds_dwordx4 v182, s[24:25]
	v_mov_b32_e32 v182, v137
	s_mov_b32 m0, s36
	s_nop 0
	global_load_lds_dwordx4 v182, s[24:25]
	s_waitcnt vmcnt(8)
	s_waitcnt lgkmcnt(0)
	s_barrier
	v_mfma_f32_16x16x128_f8f6f4 v[60:63], v[138:145], v[64:71], v[60:63]
	v_mfma_f32_16x16x128_f8f6f4 v[56:59], v[146:153], v[64:71], v[56:59]
	v_mfma_f32_16x16x128_f8f6f4 v[228:231], v[138:145], v[72:79], v[44:47]
	v_mfma_f32_16x16x128_f8f6f4 v[232:235], v[146:153], v[72:79], v[40:43]
	v_mfma_f32_16x16x128_f8f6f4 v[236:239], v[138:145], v[80:87], v[28:31]
	v_mfma_f32_16x16x128_f8f6f4 v[240:243], v[146:153], v[80:87], v[24:27]
	v_mfma_f32_16x16x128_f8f6f4 v[248:251], v[138:145], v[88:95], v[12:15]
	v_mfma_f32_16x16x128_f8f6f4 v[186:189], v[146:153], v[88:95], v[8:11]
	v_mfma_f32_16x16x128_f8f6f4 v[52:55], v[154:161], v[64:71], v[52:55]
	v_mfma_f32_16x16x128_f8f6f4 v[48:51], v[162:169], v[64:71], v[48:51]
	v_mfma_f32_16x16x128_f8f6f4 v[190:193], v[154:161], v[72:79], v[36:39]
	v_mfma_f32_16x16x128_f8f6f4 v[210:213], v[162:169], v[72:79], v[32:35]
	v_mfma_f32_16x16x128_f8f6f4 v[206:209], v[154:161], v[80:87], v[20:23]
	v_mfma_f32_16x16x128_f8f6f4 v[214:217], v[162:169], v[80:87], v[16:19]
	v_mfma_f32_16x16x128_f8f6f4 v[222:225], v[154:161], v[88:95], v[4:7]
	v_mfma_f32_16x16x128_f8f6f4 v[218:221], v[162:169], v[88:95], v[0:3]
	s_barrier
	s_nop 4
	ds_read_b128 v[0:3], v134 offset:32768
	ds_read_b128 v[16:19], v134 offset:34816
	ds_read_b128 v[4:7], v135 offset:32768
	ds_read_b128 v[20:23], v135 offset:34816
	ds_read_b128 v[138:141], v134 offset:49152
	ds_read_b128 v[146:149], v134 offset:51200
	ds_read_b128 v[142:145], v135 offset:49152
	ds_read_b128 v[150:153], v135 offset:51200
	s_add_u32 s64, s24, 0x20000
	v_mov_b32_e32 v64, v136
	s_mov_b32 m0, s37
	ds_read_b128 v[8:11], v132 offset:32768
	ds_read_b128 v[24:27], v132 offset:34816
	ds_read_b128 v[12:15], v133 offset:32768
	ds_read_b128 v[28:31], v133 offset:34816
	ds_read_b128 v[32:35], v132 offset:36864
	ds_read_b128 v[40:43], v132 offset:38912
	ds_read_b128 v[36:39], v133 offset:36864
	ds_read_b128 v[44:47], v133 offset:38912
	s_addc_u32 s65, s25, 0
	s_nop 0
	global_load_lds_dwordx4 v64, s[64:65]
	v_mov_b32_e32 v64, v137
	s_mov_b32 m0, s38
	s_nop 0
	global_load_lds_dwordx4 v64, s[64:65]
	s_waitcnt vmcnt(8)
	s_waitcnt lgkmcnt(0)
	s_barrier
	v_mfma_f32_16x16x128_f8f6f4 v[124:127], v[0:7], v[8:15], v[124:127]
	v_mfma_f32_16x16x128_f8f6f4 v[120:123], v[16:23], v[8:15], v[120:123]
	v_mfma_f32_16x16x128_f8f6f4 v[108:111], v[0:7], v[24:31], v[108:111]
	v_mfma_f32_16x16x128_f8f6f4 v[104:107], v[16:23], v[24:31], v[104:107]
	v_mfma_f32_16x16x128_f8f6f4 v[92:95], v[0:7], v[32:39], v[128:131]
	v_mfma_f32_16x16x128_f8f6f4 v[88:91], v[16:23], v[32:39], v[178:181]
	v_mfma_f32_16x16x128_f8f6f4 v[76:79], v[0:7], v[40:47], v[202:205]
	v_mfma_f32_16x16x128_f8f6f4 v[72:75], v[16:23], v[40:47], v[244:247]
	v_mfma_f32_16x16x128_f8f6f4 v[116:119], v[138:145], v[8:15], v[116:119]
	v_mfma_f32_16x16x128_f8f6f4 v[112:115], v[146:153], v[8:15], v[112:115]
	v_mfma_f32_16x16x128_f8f6f4 v[100:103], v[138:145], v[24:31], v[100:103]
	v_mfma_f32_16x16x128_f8f6f4 v[96:99], v[146:153], v[24:31], v[96:99]
	v_mfma_f32_16x16x128_f8f6f4 v[84:87], v[138:145], v[32:39], v[170:173]
	v_mfma_f32_16x16x128_f8f6f4 v[80:83], v[146:153], v[32:39], v[174:177]
	v_mfma_f32_16x16x128_f8f6f4 v[68:71], v[138:145], v[40:47], v[194:197]
	v_mfma_f32_16x16x128_f8f6f4 v[64:67], v[146:153], v[40:47], v[198:201]
	s_barrier
	v_mov_b32_e32 v184, v136
	ds_read_b128 v[32:35], v132 offset:49152
	ds_read_b128 v[154:157], v132 offset:51200
	ds_read_b128 v[36:39], v133 offset:49152
	ds_read_b128 v[158:161], v133 offset:51200
	ds_read_b128 v[162:165], v132 offset:53248
	ds_read_b128 v[170:173], v132 offset:55296
	ds_read_b128 v[166:169], v133 offset:53248
	ds_read_b128 v[174:177], v133 offset:55296
	s_mov_b32 m0, s42
	v_lshl_add_u64 v[8:9], s[26:27], 0, v[184:185]
	v_lshl_add_u64 v[8:9], v[8:9], 0, s[46:47]
	v_mov_b32_e32 v184, v137
	global_load_lds_dwordx4 v[8:9], off
	s_mov_b32 m0, s43
	v_lshl_add_u64 v[8:9], s[26:27], 0, v[184:185]
	v_lshl_add_u64 v[8:9], v[8:9], 0, s[46:47]
	global_load_lds_dwordx4 v[8:9], off
	s_add_u32 s26, s26, 0x20080
	v_mov_b32_e32 v8, v136
	s_addc_u32 s27, s27, 0
	s_mov_b32 m0, s50
	v_mov_b32_e32 v184, v136
	global_load_lds_dwordx4 v8, s[26:27]
	v_mov_b32_e32 v8, v137
	s_mov_b32 m0, s51
	s_nop 0
	global_load_lds_dwordx4 v8, s[26:27]
	s_mov_b32 m0, s44
	v_lshl_add_u64 v[8:9], s[24:25], 0, v[184:185]
	v_lshl_add_u64 v[8:9], v[8:9], 0, s[46:47]
	v_mov_b32_e32 v184, v137
	global_load_lds_dwordx4 v[8:9], off
	s_mov_b32 m0, s49
	v_lshl_add_u64 v[8:9], s[24:25], 0, v[184:185]
	v_lshl_add_u64 v[8:9], v[8:9], 0, s[46:47]
	global_load_lds_dwordx4 v[8:9], off
	s_waitcnt vmcnt(8)
	s_waitcnt lgkmcnt(0)
	s_barrier
	v_mfma_f32_16x16x128_f8f6f4 v[60:63], v[0:7], v[32:39], v[60:63]
	v_mfma_f32_16x16x128_f8f6f4 v[56:59], v[16:23], v[32:39], v[56:59]
	v_mfma_f32_16x16x128_f8f6f4 v[44:47], v[0:7], v[154:161], v[228:231]
	v_mfma_f32_16x16x128_f8f6f4 v[40:43], v[16:23], v[154:161], v[232:235]
	v_mfma_f32_16x16x128_f8f6f4 v[28:31], v[0:7], v[162:169], v[236:239]
	v_mfma_f32_16x16x128_f8f6f4 v[24:27], v[16:23], v[162:169], v[240:243]
	v_mfma_f32_16x16x128_f8f6f4 v[12:15], v[0:7], v[170:177], v[248:251]
	v_mfma_f32_16x16x128_f8f6f4 v[8:11], v[16:23], v[170:177], v[186:189]
	v_mfma_f32_16x16x128_f8f6f4 v[52:55], v[138:145], v[32:39], v[52:55]
	v_mfma_f32_16x16x128_f8f6f4 v[48:51], v[146:153], v[32:39], v[48:51]
	v_mfma_f32_16x16x128_f8f6f4 v[36:39], v[138:145], v[154:161], v[190:193]
	v_mfma_f32_16x16x128_f8f6f4 v[32:35], v[146:153], v[154:161], v[210:213]
	v_mfma_f32_16x16x128_f8f6f4 v[20:23], v[138:145], v[162:169], v[206:209]
	v_mfma_f32_16x16x128_f8f6f4 v[16:19], v[146:153], v[162:169], v[214:217]
	v_mfma_f32_16x16x128_f8f6f4 v[4:7], v[138:145], v[170:177], v[222:225]
	v_mfma_f32_16x16x128_f8f6f4 v[0:3], v[146:153], v[170:177], v[218:221]
	s_barrier
	s_add_i32 s28, s28, 2
	s_add_u32 s22, s22, 0x100
	s_addc_u32 s23, s23, 0
	s_add_u32 s17, s17, 0x100
	s_addc_u32 s19, s19, 0
	s_cmp_gt_u32 s28, 5
	s_cbranch_scc0 .LBB0_244
	s_and_b64 vcc, exec, s[14:15]
	s_cbranch_vccz .LBB0_247
	s_barrier

.LBB0_750:
	s_ashr_i32 s19, s18, 31
	s_lshl_b64 s[20:21], s[18:19], 18
	s_add_u32 s20, s33, s20
	s_addc_u32 s21, s34, s21
	s_and_b64 s[22:23], s[2:3], exec
	s_cselect_b32 s5, s21, s27
	s_cselect_b32 s19, s20, s26
	s_ashr_i32 s17, s16, 31
	s_lshl_b64 s[22:23], s[16:17], 18
	s_add_u32 s22, s35, s22
	s_addc_u32 s23, s36, s23
	s_and_b64 s[30:31], s[2:3], exec
	s_cselect_b32 s17, s23, s29
	s_cselect_b32 s25, s22, s28
	s_add_u32 s26, s26, 0x20080
	s_addc_u32 s27, s27, 0
	s_add_u32 s68, s28, 0x100
	v_mov_b32_e32 v183, 0x1200
	s_addc_u32 s70, s29, 0
	s_mov_b32 s72, -2
	ds_read_b128 v[128:131], v162
	ds_read_b128 v[136:139], v162 offset:2048
	ds_read_b128 v[132:135], v163
	ds_read_b128 v[140:143], v163 offset:2048
	ds_read_b128 v[144:147], v162 offset:16384
	ds_read_b128 v[152:155], v162 offset:18432
	ds_read_b128 v[148:151], v163 offset:16384
	ds_read_b128 v[156:159], v163 offset:18432
	s_add_u32 s28, s26, 0xfffe0080
	s_addc_u32 s29, s27, -1
	s_cmp_eq_u32 s72, 4
	s_cselect_b32 s29, s5, s29
	s_cselect_b32 s28, s19, s28
	s_cselect_b32 s31, s17, s70
	s_cselect_b32 s30, s25, s68
	v_mov_b32_e32 v182, v164
	ds_read_b128 v[166:169], v160
	ds_read_b128 v[174:177], v160 offset:2048
	ds_read_b128 v[170:173], v161
	ds_read_b128 v[178:181], v161 offset:2048
	ds_read_b128 v[194:197], v160 offset:4096
	ds_read_b128 v[228:231], v160 offset:6144
	ds_read_b128 v[198:201], v161 offset:4096
	ds_read_b128 v[232:235], v161 offset:6144
	s_add_i32 m0, s37, 0xc000
	s_nop 0
	global_load_lds_dwordx4 v182, s[26:27]
	v_mov_b32_e32 v182, v165
	s_add_i32 m0, s37, 0xe000
	s_nop 0
	global_load_lds_dwordx4 v182, s[26:27]
	s_waitcnt vmcnt(8)
	s_waitcnt lgkmcnt(0)
	s_barrier
	v_mfma_f32_16x16x128_f8f6f4 v[124:127], v[128:135], v[166:173], 0
	v_mfma_f32_16x16x128_f8f6f4 v[120:123], v[136:143], v[166:173], 0
	v_mfma_f32_16x16x128_f8f6f4 v[108:111], v[128:135], v[174:181], 0
	v_mfma_f32_16x16x128_f8f6f4 v[104:107], v[136:143], v[174:181], 0
	v_mfma_f32_16x16x128_f8f6f4 v[186:189], v[128:135], v[194:201], 0
	v_mfma_f32_16x16x128_f8f6f4 v[190:193], v[136:143], v[194:201], 0
	v_mfma_f32_16x16x128_f8f6f4 v[202:205], v[128:135], v[228:235], 0
	v_mfma_f32_16x16x128_f8f6f4 v[206:209], v[136:143], v[228:235], 0
	v_mfma_f32_16x16x128_f8f6f4 v[116:119], v[144:151], v[166:173], 0
	v_mfma_f32_16x16x128_f8f6f4 v[112:115], v[152:159], v[166:173], 0
	v_mfma_f32_16x16x128_f8f6f4 v[100:103], v[144:151], v[174:181], 0
	v_mfma_f32_16x16x128_f8f6f4 v[96:99], v[152:159], v[174:181], 0
	v_mfma_f32_16x16x128_f8f6f4 v[166:169], v[144:151], v[194:201], 0
	v_mfma_f32_16x16x128_f8f6f4 v[170:173], v[152:159], v[194:201], 0
	v_mfma_f32_16x16x128_f8f6f4 v[174:177], v[144:151], v[228:235], 0
	v_mfma_f32_16x16x128_f8f6f4 v[178:181], v[152:159], v[228:235], 0
	s_barrier
	v_mov_b32_e32 v182, v164
	s_mov_b32 m0, s38
	s_nop 2
	ds_read_b128 v[64:67], v160 offset:16384
	ds_read_b128 v[72:75], v160 offset:18432
	ds_read_b128 v[68:71], v161 offset:16384
	ds_read_b128 v[76:79], v161 offset:18432
	ds_read_b128 v[80:83], v160 offset:20480
	ds_read_b128 v[88:91], v160 offset:22528
	ds_read_b128 v[84:87], v161 offset:20480
	ds_read_b128 v[92:95], v161 offset:22528
	s_add_u32 s74, s30, 0x20000
	global_load_lds_dwordx4 v182, s[30:31]
	v_mov_b32_e32 v182, v165
	s_mov_b32 m0, s39
	s_addc_u32 s75, s31, 0
	global_load_lds_dwordx4 v182, s[30:31]
	v_mov_b32_e32 v182, v164
	s_mov_b32 m0, s40
	s_nop 0
	global_load_lds_dwordx4 v182, s[74:75]
	v_mov_b32_e32 v182, v165
	s_mov_b32 m0, s42
	s_nop 0
	global_load_lds_dwordx4 v182, s[74:75]
	v_mov_b32_e32 v182, v164
	s_mov_b32 m0, s37
	s_nop 0
	global_load_lds_dwordx4 v182, s[28:29]
	v_mov_b32_e32 v182, v165
	s_mov_b32 m0, s43
	s_nop 0
	global_load_lds_dwordx4 v182, s[28:29]
	s_waitcnt vmcnt(8)
	s_waitcnt lgkmcnt(0)
	s_barrier
	v_mfma_f32_16x16x128_f8f6f4 v[60:63], v[128:135], v[64:71], 0
	v_mfma_f32_16x16x128_f8f6f4 v[56:59], v[136:143], v[64:71], 0
	v_mfma_f32_16x16x128_f8f6f4 v[194:197], v[128:135], v[72:79], 0
	v_mfma_f32_16x16x128_f8f6f4 v[198:201], v[136:143], v[72:79], 0
	v_mfma_f32_16x16x128_f8f6f4 v[210:213], v[128:135], v[80:87], 0
	v_mfma_f32_16x16x128_f8f6f4 v[214:217], v[136:143], v[80:87], 0
	v_mfma_f32_16x16x128_f8f6f4 v[218:221], v[128:135], v[88:95], 0
	v_mfma_f32_16x16x128_f8f6f4 v[222:225], v[136:143], v[88:95], 0
	v_mfma_f32_16x16x128_f8f6f4 v[52:55], v[144:151], v[64:71], 0
	v_mfma_f32_16x16x128_f8f6f4 v[48:51], v[152:159], v[64:71], 0
	v_mfma_f32_16x16x128_f8f6f4 v[228:231], v[144:151], v[72:79], 0
	v_mfma_f32_16x16x128_f8f6f4 v[232:235], v[152:159], v[72:79], 0
	v_mfma_f32_16x16x128_f8f6f4 v[236:239], v[144:151], v[80:87], 0
	v_mfma_f32_16x16x128_f8f6f4 v[240:243], v[152:159], v[80:87], 0
	v_mfma_f32_16x16x128_f8f6f4 v[244:247], v[144:151], v[88:95], 0
	v_mfma_f32_16x16x128_f8f6f4 v[248:251], v[152:159], v[88:95], 0
	s_barrier
	s_nop 4
	ds_read_b128 v[0:3], v162 offset:32768
	ds_read_b128 v[16:19], v162 offset:34816
	ds_read_b128 v[4:7], v163 offset:32768
	ds_read_b128 v[20:23], v163 offset:34816
	ds_read_b128 v[128:131], v162 offset:49152
	ds_read_b128 v[136:139], v162 offset:51200
	ds_read_b128 v[132:135], v163 offset:49152
	ds_read_b128 v[140:143], v163 offset:51200
	s_add_u32 s74, s28, 0x20000
	v_mov_b32_e32 v64, v164
	s_mov_b32 m0, s44
	ds_read_b128 v[8:11], v160 offset:32768
	ds_read_b128 v[24:27], v160 offset:34816
	ds_read_b128 v[12:15], v161 offset:32768
	ds_read_b128 v[28:31], v161 offset:34816
	ds_read_b128 v[32:35], v160 offset:36864
	ds_read_b128 v[40:43], v160 offset:38912
	ds_read_b128 v[36:39], v161 offset:36864
	ds_read_b128 v[44:47], v161 offset:38912
	s_addc_u32 s75, s29, 0
	s_nop 0
	global_load_lds_dwordx4 v64, s[74:75]
	v_mov_b32_e32 v64, v165
	s_mov_b32 m0, s49
	s_nop 0
	global_load_lds_dwordx4 v64, s[74:75]
	s_waitcnt vmcnt(8)
	s_waitcnt lgkmcnt(0)
	s_barrier
	v_mfma_f32_16x16x128_f8f6f4 v[124:127], v[0:7], v[8:15], v[124:127]
	v_mfma_f32_16x16x128_f8f6f4 v[120:123], v[16:23], v[8:15], v[120:123]
	v_mfma_f32_16x16x128_f8f6f4 v[108:111], v[0:7], v[24:31], v[108:111]
	v_mfma_f32_16x16x128_f8f6f4 v[104:107], v[16:23], v[24:31], v[104:107]
	v_mfma_f32_16x16x128_f8f6f4 v[92:95], v[0:7], v[32:39], v[186:189]
	v_mfma_f32_16x16x128_f8f6f4 v[88:91], v[16:23], v[32:39], v[190:193]
	v_mfma_f32_16x16x128_f8f6f4 v[76:79], v[0:7], v[40:47], v[202:205]
	v_mfma_f32_16x16x128_f8f6f4 v[72:75], v[16:23], v[40:47], v[206:209]
	v_mfma_f32_16x16x128_f8f6f4 v[116:119], v[128:135], v[8:15], v[116:119]
	v_mfma_f32_16x16x128_f8f6f4 v[112:115], v[136:143], v[8:15], v[112:115]
	v_mfma_f32_16x16x128_f8f6f4 v[100:103], v[128:135], v[24:31], v[100:103]
	v_mfma_f32_16x16x128_f8f6f4 v[96:99], v[136:143], v[24:31], v[96:99]
	v_mfma_f32_16x16x128_f8f6f4 v[84:87], v[128:135], v[32:39], v[166:169]
	v_mfma_f32_16x16x128_f8f6f4 v[80:83], v[136:143], v[32:39], v[170:173]
	v_mfma_f32_16x16x128_f8f6f4 v[68:71], v[128:135], v[40:47], v[174:177]
	v_mfma_f32_16x16x128_f8f6f4 v[64:67], v[136:143], v[40:47], v[178:181]
	s_barrier
	v_mov_b32_e32 v184, v164
	ds_read_b128 v[32:35], v160 offset:49152
	ds_read_b128 v[144:147], v160 offset:51200
	ds_read_b128 v[36:39], v161 offset:49152
	ds_read_b128 v[148:151], v161 offset:51200
	ds_read_b128 v[152:155], v160 offset:53248
	ds_read_b128 v[166:169], v160 offset:55296
	ds_read_b128 v[156:159], v161 offset:53248
	ds_read_b128 v[170:173], v161 offset:55296
	s_mov_b32 m0, s54
	v_lshl_add_u64 v[8:9], s[30:31], 0, v[184:185]
	v_lshl_add_u64 v[8:9], v[8:9], 0, s[46:47]
	v_mov_b32_e32 v184, v165
	global_load_lds_dwordx4 v[8:9], off
	s_mov_b32 m0, s55
	v_lshl_add_u64 v[8:9], s[30:31], 0, v[184:185]
	v_lshl_add_u64 v[8:9], v[8:9], 0, s[46:47]
	global_load_lds_dwordx4 v[8:9], off
	s_add_u32 s30, s30, 0x20080
	v_mov_b32_e32 v8, v164
	s_addc_u32 s31, s31, 0
	s_mov_b32 m0, s59
	v_mov_b32_e32 v184, v164
	global_load_lds_dwordx4 v8, s[30:31]
	v_mov_b32_e32 v8, v165
	s_mov_b32 m0, s64
	s_nop 0
	global_load_lds_dwordx4 v8, s[30:31]
	s_mov_b32 m0, s56
	v_lshl_add_u64 v[8:9], s[28:29], 0, v[184:185]
	v_lshl_add_u64 v[8:9], v[8:9], 0, s[46:47]
	v_mov_b32_e32 v184, v165
	global_load_lds_dwordx4 v[8:9], off
	s_mov_b32 m0, s57
	v_lshl_add_u64 v[8:9], s[28:29], 0, v[184:185]
	v_lshl_add_u64 v[8:9], v[8:9], 0, s[46:47]
	global_load_lds_dwordx4 v[8:9], off
	s_waitcnt vmcnt(8)
	s_waitcnt lgkmcnt(0)
	s_barrier
	v_mfma_f32_16x16x128_f8f6f4 v[60:63], v[0:7], v[32:39], v[60:63]
	v_mfma_f32_16x16x128_f8f6f4 v[56:59], v[16:23], v[32:39], v[56:59]
	v_mfma_f32_16x16x128_f8f6f4 v[44:47], v[0:7], v[144:151], v[194:197]
	v_mfma_f32_16x16x128_f8f6f4 v[40:43], v[16:23], v[144:151], v[198:201]
	v_mfma_f32_16x16x128_f8f6f4 v[28:31], v[0:7], v[152:159], v[210:213]
	v_mfma_f32_16x16x128_f8f6f4 v[24:27], v[16:23], v[152:159], v[214:217]
	v_mfma_f32_16x16x128_f8f6f4 v[12:15], v[0:7], v[166:173], v[218:221]
	v_mfma_f32_16x16x128_f8f6f4 v[8:11], v[16:23], v[166:173], v[222:225]
	v_mfma_f32_16x16x128_f8f6f4 v[52:55], v[128:135], v[32:39], v[52:55]
	v_mfma_f32_16x16x128_f8f6f4 v[48:51], v[136:143], v[32:39], v[48:51]
	v_mfma_f32_16x16x128_f8f6f4 v[36:39], v[128:135], v[144:151], v[228:231]
	v_mfma_f32_16x16x128_f8f6f4 v[32:35], v[136:143], v[144:151], v[232:235]
	v_mfma_f32_16x16x128_f8f6f4 v[20:23], v[128:135], v[152:159], v[236:239]
	v_mfma_f32_16x16x128_f8f6f4 v[16:19], v[136:143], v[152:159], v[240:243]
	v_mfma_f32_16x16x128_f8f6f4 v[4:7], v[128:135], v[166:173], v[244:247]
	v_mfma_f32_16x16x128_f8f6f4 v[0:3], v[136:143], v[166:173], v[248:251]
	s_barrier
	s_add_i32 s72, s72, 2
	s_add_u32 s26, s26, 0x100
	s_addc_u32 s27, s27, 0
	s_add_u32 s68, s68, 0x100
	s_addc_u32 s70, s70, 0
.LBB0_751:
	ds_read_b128 v[128:131], v162
	ds_read_b128 v[136:139], v162 offset:2048
	ds_read_b128 v[132:135], v163
	ds_read_b128 v[140:143], v163 offset:2048
	ds_read_b128 v[144:147], v162 offset:16384
	ds_read_b128 v[152:155], v162 offset:18432
	ds_read_b128 v[148:151], v163 offset:16384
	ds_read_b128 v[156:159], v163 offset:18432
	s_add_u32 s28, s26, 0xfffe0080
	s_addc_u32 s29, s27, -1
	s_cmp_eq_u32 s72, 4
	s_cselect_b32 s29, s5, s29
	s_cselect_b32 s28, s19, s28
	s_cselect_b32 s31, s17, s70
	s_cselect_b32 s30, s25, s68
	v_mov_b32_e32 v182, v164
	ds_read_b128 v[166:169], v160
	ds_read_b128 v[174:177], v160 offset:2048
	ds_read_b128 v[170:173], v161
	ds_read_b128 v[178:181], v161 offset:2048
	ds_read_b128 v[194:197], v160 offset:4096
	ds_read_b128 v[228:231], v160 offset:6144
	ds_read_b128 v[198:201], v161 offset:4096
	ds_read_b128 v[232:235], v161 offset:6144
	s_add_i32 m0, s37, 0xc000
	s_nop 0
	global_load_lds_dwordx4 v182, s[26:27]
	v_mov_b32_e32 v182, v165
	s_add_i32 m0, s37, 0xe000
	s_nop 0
	global_load_lds_dwordx4 v182, s[26:27]
	s_waitcnt vmcnt(8)
	s_waitcnt lgkmcnt(0)
	s_barrier
	v_mfma_f32_16x16x128_f8f6f4 v[124:127], v[128:135], v[166:173], v[124:127]
	v_mfma_f32_16x16x128_f8f6f4 v[120:123], v[136:143], v[166:173], v[120:123]
	v_mfma_f32_16x16x128_f8f6f4 v[108:111], v[128:135], v[174:181], v[108:111]
	v_mfma_f32_16x16x128_f8f6f4 v[104:107], v[136:143], v[174:181], v[104:107]
	v_mfma_f32_16x16x128_f8f6f4 v[186:189], v[128:135], v[194:201], v[92:95]
	v_mfma_f32_16x16x128_f8f6f4 v[190:193], v[136:143], v[194:201], v[88:91]
	v_mfma_f32_16x16x128_f8f6f4 v[202:205], v[128:135], v[228:235], v[76:79]
	v_mfma_f32_16x16x128_f8f6f4 v[206:209], v[136:143], v[228:235], v[72:75]
	v_mfma_f32_16x16x128_f8f6f4 v[116:119], v[144:151], v[166:173], v[116:119]
	v_mfma_f32_16x16x128_f8f6f4 v[112:115], v[152:159], v[166:173], v[112:115]
	v_mfma_f32_16x16x128_f8f6f4 v[100:103], v[144:151], v[174:181], v[100:103]
	v_mfma_f32_16x16x128_f8f6f4 v[96:99], v[152:159], v[174:181], v[96:99]
	v_mfma_f32_16x16x128_f8f6f4 v[166:169], v[144:151], v[194:201], v[84:87]
	v_mfma_f32_16x16x128_f8f6f4 v[170:173], v[152:159], v[194:201], v[80:83]
	v_mfma_f32_16x16x128_f8f6f4 v[174:177], v[144:151], v[228:235], v[68:71]
	v_mfma_f32_16x16x128_f8f6f4 v[178:181], v[152:159], v[228:235], v[64:67]
	s_barrier
	v_mov_b32_e32 v182, v164
	s_mov_b32 m0, s38
	s_nop 2
	ds_read_b128 v[64:67], v160 offset:16384
	ds_read_b128 v[72:75], v160 offset:18432
	ds_read_b128 v[68:71], v161 offset:16384
	ds_read_b128 v[76:79], v161 offset:18432
	ds_read_b128 v[80:83], v160 offset:20480
	ds_read_b128 v[88:91], v160 offset:22528
	ds_read_b128 v[84:87], v161 offset:20480
	ds_read_b128 v[92:95], v161 offset:22528
	s_add_u32 s74, s30, 0x20000
	global_load_lds_dwordx4 v182, s[30:31]
	v_mov_b32_e32 v182, v165
	s_mov_b32 m0, s39
	s_addc_u32 s75, s31, 0
	global_load_lds_dwordx4 v182, s[30:31]
	v_mov_b32_e32 v182, v164
	s_mov_b32 m0, s40
	s_nop 0
	global_load_lds_dwordx4 v182, s[74:75]
	v_mov_b32_e32 v182, v165
	s_mov_b32 m0, s42
	s_nop 0
	global_load_lds_dwordx4 v182, s[74:75]
	v_mov_b32_e32 v182, v164
	s_mov_b32 m0, s37
	s_nop 0
	global_load_lds_dwordx4 v182, s[28:29]
	v_mov_b32_e32 v182, v165
	s_mov_b32 m0, s43
	s_nop 0
	global_load_lds_dwordx4 v182, s[28:29]
	s_waitcnt vmcnt(8)
	s_waitcnt lgkmcnt(0)
	s_barrier
	v_mfma_f32_16x16x128_f8f6f4 v[60:63], v[128:135], v[64:71], v[60:63]
	v_mfma_f32_16x16x128_f8f6f4 v[56:59], v[136:143], v[64:71], v[56:59]
	v_mfma_f32_16x16x128_f8f6f4 v[194:197], v[128:135], v[72:79], v[44:47]
	v_mfma_f32_16x16x128_f8f6f4 v[198:201], v[136:143], v[72:79], v[40:43]
	v_mfma_f32_16x16x128_f8f6f4 v[210:213], v[128:135], v[80:87], v[28:31]
	v_mfma_f32_16x16x128_f8f6f4 v[214:217], v[136:143], v[80:87], v[24:27]
	v_mfma_f32_16x16x128_f8f6f4 v[218:221], v[128:135], v[88:95], v[12:15]
	v_mfma_f32_16x16x128_f8f6f4 v[222:225], v[136:143], v[88:95], v[8:11]
	v_mfma_f32_16x16x128_f8f6f4 v[52:55], v[144:151], v[64:71], v[52:55]
	v_mfma_f32_16x16x128_f8f6f4 v[48:51], v[152:159], v[64:71], v[48:51]
	v_mfma_f32_16x16x128_f8f6f4 v[228:231], v[144:151], v[72:79], v[36:39]
	v_mfma_f32_16x16x128_f8f6f4 v[232:235], v[152:159], v[72:79], v[32:35]
	v_mfma_f32_16x16x128_f8f6f4 v[236:239], v[144:151], v[80:87], v[20:23]
	v_mfma_f32_16x16x128_f8f6f4 v[240:243], v[152:159], v[80:87], v[16:19]
	v_mfma_f32_16x16x128_f8f6f4 v[244:247], v[144:151], v[88:95], v[4:7]
	v_mfma_f32_16x16x128_f8f6f4 v[248:251], v[152:159], v[88:95], v[0:3]
	s_barrier
	s_nop 4
	ds_read_b128 v[0:3], v162 offset:32768
	ds_read_b128 v[16:19], v162 offset:34816
	ds_read_b128 v[4:7], v163 offset:32768
	ds_read_b128 v[20:23], v163 offset:34816
	ds_read_b128 v[128:131], v162 offset:49152
	ds_read_b128 v[136:139], v162 offset:51200
	ds_read_b128 v[132:135], v163 offset:49152
	ds_read_b128 v[140:143], v163 offset:51200
	s_add_u32 s74, s28, 0x20000
	v_mov_b32_e32 v64, v164
	s_mov_b32 m0, s44
	ds_read_b128 v[8:11], v160 offset:32768
	ds_read_b128 v[24:27], v160 offset:34816
	ds_read_b128 v[12:15], v161 offset:32768
	ds_read_b128 v[28:31], v161 offset:34816
	ds_read_b128 v[32:35], v160 offset:36864
	ds_read_b128 v[40:43], v160 offset:38912
	ds_read_b128 v[36:39], v161 offset:36864
	ds_read_b128 v[44:47], v161 offset:38912
	s_addc_u32 s75, s29, 0
	s_nop 0
	global_load_lds_dwordx4 v64, s[74:75]
	v_mov_b32_e32 v64, v165
	s_mov_b32 m0, s49
	s_nop 0
	global_load_lds_dwordx4 v64, s[74:75]
	s_waitcnt vmcnt(8)
	s_waitcnt lgkmcnt(0)
	s_barrier
	v_mfma_f32_16x16x128_f8f6f4 v[124:127], v[0:7], v[8:15], v[124:127]
	v_mfma_f32_16x16x128_f8f6f4 v[120:123], v[16:23], v[8:15], v[120:123]
	v_mfma_f32_16x16x128_f8f6f4 v[108:111], v[0:7], v[24:31], v[108:111]
	v_mfma_f32_16x16x128_f8f6f4 v[104:107], v[16:23], v[24:31], v[104:107]
	v_mfma_f32_16x16x128_f8f6f4 v[92:95], v[0:7], v[32:39], v[186:189]
	v_mfma_f32_16x16x128_f8f6f4 v[88:91], v[16:23], v[32:39], v[190:193]
	v_mfma_f32_16x16x128_f8f6f4 v[76:79], v[0:7], v[40:47], v[202:205]
	v_mfma_f32_16x16x128_f8f6f4 v[72:75], v[16:23], v[40:47], v[206:209]
	v_mfma_f32_16x16x128_f8f6f4 v[116:119], v[128:135], v[8:15], v[116:119]
	v_mfma_f32_16x16x128_f8f6f4 v[112:115], v[136:143], v[8:15], v[112:115]
	v_mfma_f32_16x16x128_f8f6f4 v[100:103], v[128:135], v[24:31], v[100:103]
	v_mfma_f32_16x16x128_f8f6f4 v[96:99], v[136:143], v[24:31], v[96:99]
	v_mfma_f32_16x16x128_f8f6f4 v[84:87], v[128:135], v[32:39], v[166:169]
	v_mfma_f32_16x16x128_f8f6f4 v[80:83], v[136:143], v[32:39], v[170:173]
	v_mfma_f32_16x16x128_f8f6f4 v[68:71], v[128:135], v[40:47], v[174:177]
	v_mfma_f32_16x16x128_f8f6f4 v[64:67], v[136:143], v[40:47], v[178:181]
	s_barrier
	v_mov_b32_e32 v184, v164
	ds_read_b128 v[32:35], v160 offset:49152
	ds_read_b128 v[144:147], v160 offset:51200
	ds_read_b128 v[36:39], v161 offset:49152
	ds_read_b128 v[148:151], v161 offset:51200
	ds_read_b128 v[152:155], v160 offset:53248
	ds_read_b128 v[166:169], v160 offset:55296
	ds_read_b128 v[156:159], v161 offset:53248
	ds_read_b128 v[170:173], v161 offset:55296
	s_mov_b32 m0, s54
	v_lshl_add_u64 v[8:9], s[30:31], 0, v[184:185]
	v_lshl_add_u64 v[8:9], v[8:9], 0, s[46:47]
	v_mov_b32_e32 v184, v165
	global_load_lds_dwordx4 v[8:9], off
	s_mov_b32 m0, s55
	v_lshl_add_u64 v[8:9], s[30:31], 0, v[184:185]
	v_lshl_add_u64 v[8:9], v[8:9], 0, s[46:47]
	global_load_lds_dwordx4 v[8:9], off
	s_add_u32 s30, s30, 0x20080
	v_mov_b32_e32 v8, v164
	s_addc_u32 s31, s31, 0
	s_mov_b32 m0, s59
	v_mov_b32_e32 v184, v164
	global_load_lds_dwordx4 v8, s[30:31]
	v_mov_b32_e32 v8, v165
	s_mov_b32 m0, s64
	s_nop 0
	global_load_lds_dwordx4 v8, s[30:31]
	s_mov_b32 m0, s56
	v_lshl_add_u64 v[8:9], s[28:29], 0, v[184:185]
	v_lshl_add_u64 v[8:9], v[8:9], 0, s[46:47]
	v_mov_b32_e32 v184, v165
	global_load_lds_dwordx4 v[8:9], off
	s_mov_b32 m0, s57
	v_lshl_add_u64 v[8:9], s[28:29], 0, v[184:185]
	v_lshl_add_u64 v[8:9], v[8:9], 0, s[46:47]
	global_load_lds_dwordx4 v[8:9], off
	s_waitcnt vmcnt(8)
	s_waitcnt lgkmcnt(0)
	s_barrier
	v_mfma_f32_16x16x128_f8f6f4 v[60:63], v[0:7], v[32:39], v[60:63]
	v_mfma_f32_16x16x128_f8f6f4 v[56:59], v[16:23], v[32:39], v[56:59]
	v_mfma_f32_16x16x128_f8f6f4 v[44:47], v[0:7], v[144:151], v[194:197]
	v_mfma_f32_16x16x128_f8f6f4 v[40:43], v[16:23], v[144:151], v[198:201]
	v_mfma_f32_16x16x128_f8f6f4 v[28:31], v[0:7], v[152:159], v[210:213]
	v_mfma_f32_16x16x128_f8f6f4 v[24:27], v[16:23], v[152:159], v[214:217]
	v_mfma_f32_16x16x128_f8f6f4 v[12:15], v[0:7], v[166:173], v[218:221]
	v_mfma_f32_16x16x128_f8f6f4 v[8:11], v[16:23], v[166:173], v[222:225]
	v_mfma_f32_16x16x128_f8f6f4 v[52:55], v[128:135], v[32:39], v[52:55]
	v_mfma_f32_16x16x128_f8f6f4 v[48:51], v[136:143], v[32:39], v[48:51]
	v_mfma_f32_16x16x128_f8f6f4 v[36:39], v[128:135], v[144:151], v[228:231]
	v_mfma_f32_16x16x128_f8f6f4 v[32:35], v[136:143], v[144:151], v[232:235]
	v_mfma_f32_16x16x128_f8f6f4 v[20:23], v[128:135], v[152:159], v[236:239]
	v_mfma_f32_16x16x128_f8f6f4 v[16:19], v[136:143], v[152:159], v[240:243]
	v_mfma_f32_16x16x128_f8f6f4 v[4:7], v[128:135], v[166:173], v[244:247]
	v_mfma_f32_16x16x128_f8f6f4 v[0:3], v[136:143], v[166:173], v[248:251]
	s_barrier
	s_add_i32 s72, s72, 2
	s_add_u32 s26, s26, 0x100
	s_addc_u32 s27, s27, 0
	s_add_u32 s68, s68, 0x100
	s_addc_u32 s70, s70, 0
	s_cmp_gt_u32 s72, 5
	s_cbranch_scc0 .LBB0_751
	s_and_b64 vcc, exec, s[12:13]
	s_cbranch_vccz .LBB0_754
	s_barrier

.LBB0_1034:
	v_readfirstlane_b32 s19, v4
	s_xor_b32 s27, s75, s19
	s_lshl_b32 s19, s75, 12
	s_add_i32 s74, s19, 0
	s_add_i32 s74, s74, 0x21000
	s_add_u32 s19, s24, 0x100
	s_addc_u32 s76, s25, 0
	s_mov_b32 s77, -2
	s_mov_b64 s[24:25], s[14:15]
	ds_read_b128 v[136:139], v150
	s_waitcnt vmcnt(0)
	ds_read_b128 v[156:159], v150 offset:2048
	ds_read_b128 v[140:143], v151
	ds_read_b128 v[160:163], v151 offset:2048
	ds_read_b128 v[164:167], v150 offset:16384
	ds_read_b128 v[172:175], v150 offset:18432
	ds_read_b128 v[168:171], v151 offset:16384
	ds_read_b128 v[176:179], v151 offset:18432
	s_add_u32 s28, s24, 0x80
	s_addc_u32 s29, s25, 0
	s_cmp_eq_u32 s77, 4
	s_cselect_b32 s29, s11, s29
	s_cselect_b32 s28, s10, s28
	s_cselect_b32 s80, s27, s75
	s_cselect_b32 s37, s23, s76
	s_cselect_b32 s36, s22, s19
	ds_read_b128 v[194:197], v148
	ds_read_b128 v[228:231], v148 offset:2048
	ds_read_b128 v[198:201], v149
	ds_read_b128 v[232:235], v149 offset:2048
	ds_read_b128 v[236:239], v148 offset:4096
	ds_read_b128 v[244:247], v148 offset:6144
	ds_read_b128 v[240:243], v149 offset:4096
	ds_read_b128 v[248:251], v149 offset:6144
	v_mbcnt_lo_u32_b32 v40, -1, 0
	v_mbcnt_hi_u32_b32 v40, -1, v40
	s_mov_b32 s78, s61
	v_lshlrev_b32_e32 v40, 3, v40
	s_add_i32 m0, s35, 0xc000
	v_lshl_or_b32 v40, s78, 9, v40
	v_add_u32_e32 v40, s74, v40
	ds_read_b32 v40, v40 offset:4
	s_waitcnt lgkmcnt(0)
	v_lshlrev_b32_e32 v41, 10, v40
	v_and_or_b32 v41, v41, s69, v154
	v_bfe_u32 v40, v40, 16, 16
	v_lshl_or_b32 v40, v40, 10, v154
	global_load_lds_dwordx4 v41, s[24:25]
	s_add_i32 m0, s35, 0xe000
	s_nop 0
	global_load_lds_dwordx4 v40, s[24:25]
	s_waitcnt vmcnt(8)
	s_waitcnt lgkmcnt(0)
	s_barrier
	v_mfma_f32_16x16x128_f8f6f4 v[132:135], v[136:143], v[194:201], 0
	v_mfma_f32_16x16x128_f8f6f4 v[124:127], v[156:163], v[194:201], 0
	v_mfma_f32_16x16x128_f8f6f4 v[116:119], v[136:143], v[228:235], 0
	v_mfma_f32_16x16x128_f8f6f4 v[108:111], v[156:163], v[228:235], 0
	v_mfma_f32_16x16x128_f8f6f4 v[144:147], v[136:143], v[236:243], 0
	v_mfma_f32_16x16x128_f8f6f4 v[180:183], v[156:163], v[236:243], 0
	v_mfma_f32_16x16x128_f8f6f4 v[186:189], v[136:143], v[244:251], 0
	v_mfma_f32_16x16x128_f8f6f4 v[190:193], v[156:163], v[244:251], 0
	v_mfma_f32_16x16x128_f8f6f4 v[128:131], v[164:171], v[194:201], 0
	v_mfma_f32_16x16x128_f8f6f4 v[120:123], v[172:179], v[194:201], 0
	v_mfma_f32_16x16x128_f8f6f4 v[112:115], v[164:171], v[228:235], 0
	v_mfma_f32_16x16x128_f8f6f4 v[104:107], v[172:179], v[228:235], 0
	v_mfma_f32_16x16x128_f8f6f4 v[202:205], v[164:171], v[236:243], 0
	v_mfma_f32_16x16x128_f8f6f4 v[206:209], v[172:179], v[236:243], 0
	v_mfma_f32_16x16x128_f8f6f4 v[210:213], v[164:171], v[244:251], 0
	v_mfma_f32_16x16x128_f8f6f4 v[214:217], v[172:179], v[244:251], 0
	s_barrier
	v_mov_b32_e32 v40, v152
	s_mov_b32 m0, s44
	s_nop 2
	ds_read_b128 v[72:75], v148 offset:16384
	ds_read_b128 v[80:83], v148 offset:18432
	ds_read_b128 v[76:79], v149 offset:16384
	ds_read_b128 v[84:87], v149 offset:18432
	ds_read_b128 v[88:91], v148 offset:20480
	ds_read_b128 v[96:99], v148 offset:22528
	ds_read_b128 v[92:95], v149 offset:20480
	ds_read_b128 v[100:103], v149 offset:22528
	s_add_u32 s78, s36, 0x20000
	global_load_lds_dwordx4 v40, s[36:37]
	v_mov_b32_e32 v40, v153
	s_mov_b32 m0, s49
	s_addc_u32 s79, s37, 0
	global_load_lds_dwordx4 v40, s[36:37]
	v_mov_b32_e32 v40, v152
	s_mov_b32 m0, s50
	s_nop 0
	global_load_lds_dwordx4 v40, s[78:79]
	v_mov_b32_e32 v40, v153
	s_mov_b32 m0, s51
	s_nop 0
	global_load_lds_dwordx4 v40, s[78:79]
	v_mbcnt_lo_u32_b32 v40, -1, 0
	v_mbcnt_hi_u32_b32 v40, -1, v40
	s_mov_b32 s78, s61
	v_lshlrev_b32_e32 v40, 3, v40
	v_lshl_or_b32 v40, s78, 9, v40
	s_lshl_b32 s78, s80, 12
	s_add_i32 s78, s78, 0
	s_add_i32 s78, s78, 0x21000
	v_add_u32_e32 v40, s78, v40
	ds_read_b32 v40, v40
	s_mov_b32 m0, s35
	s_waitcnt lgkmcnt(0)
	v_lshlrev_b32_e32 v41, 10, v40
	v_and_or_b32 v41, v41, s69, v154
	v_bfe_u32 v40, v40, 16, 16
	v_lshl_or_b32 v40, v40, 10, v154
	global_load_lds_dwordx4 v41, s[28:29]
	s_mov_b32 m0, s54
	s_nop 0
	global_load_lds_dwordx4 v40, s[28:29]
	s_waitcnt vmcnt(8)
	s_waitcnt lgkmcnt(0)
	s_barrier
	v_mfma_f32_16x16x128_f8f6f4 v[48:51], v[136:143], v[80:87], 0
	v_mfma_f32_16x16x128_f8f6f4 v[36:39], v[156:163], v[80:87], 0
	v_mfma_f32_16x16x128_f8f6f4 v[28:31], v[136:143], v[88:95], 0
	v_mfma_f32_16x16x128_f8f6f4 v[20:23], v[156:163], v[88:95], 0
	v_mfma_f32_16x16x128_f8f6f4 v[12:15], v[136:143], v[96:103], 0
	v_mfma_f32_16x16x128_f8f6f4 v[4:7], v[156:163], v[96:103], 0
	v_mfma_f32_16x16x128_f8f6f4 v[40:43], v[136:143], v[72:79], 0
	v_mfma_f32_16x16x128_f8f6f4 v[52:55], v[156:163], v[72:79], 0
	v_mfma_f32_16x16x128_f8f6f4 v[64:67], v[164:171], v[72:79], 0
	v_mfma_f32_16x16x128_f8f6f4 v[56:59], v[172:179], v[72:79], 0
	v_mfma_f32_16x16x128_f8f6f4 v[44:47], v[164:171], v[80:87], 0
	v_mfma_f32_16x16x128_f8f6f4 v[32:35], v[172:179], v[80:87], 0
	v_mfma_f32_16x16x128_f8f6f4 v[24:27], v[164:171], v[88:95], 0
	v_mfma_f32_16x16x128_f8f6f4 v[16:19], v[172:179], v[88:95], 0
	v_mfma_f32_16x16x128_f8f6f4 v[8:11], v[164:171], v[96:103], 0
	v_mfma_f32_16x16x128_f8f6f4 v[0:3], v[172:179], v[96:103], 0
	s_barrier
	ds_read_b128 v[136:139], v150 offset:32768
	ds_read_b128 v[156:159], v150 offset:34816
	ds_read_b128 v[140:143], v151 offset:32768
	ds_read_b128 v[160:163], v151 offset:34816
	ds_read_b128 v[164:167], v150 offset:49152
	ds_read_b128 v[172:175], v150 offset:51200
	ds_read_b128 v[168:171], v151 offset:49152
	ds_read_b128 v[176:179], v151 offset:51200
	ds_read_b128 v[68:71], v148 offset:32768
	ds_read_b128 v[194:197], v148 offset:34816
	ds_read_b128 v[72:75], v149 offset:32768
	ds_read_b128 v[198:201], v149 offset:34816
	ds_read_b128 v[228:231], v148 offset:36864
	ds_read_b128 v[236:239], v148 offset:38912
	ds_read_b128 v[232:235], v149 offset:36864
	ds_read_b128 v[240:243], v149 offset:38912
	v_mbcnt_lo_u32_b32 v60, -1, 0
	v_mbcnt_hi_u32_b32 v60, -1, v60
	s_mov_b32 s79, s61
	v_lshlrev_b32_e32 v60, 3, v60
	s_mov_b32 m0, s55
	v_lshl_or_b32 v60, s79, 9, v60
	v_add_u32_e32 v60, s78, v60
	ds_read_b32 v60, v60 offset:4
	s_waitcnt lgkmcnt(0)
	v_lshlrev_b32_e32 v61, 10, v60
	v_and_or_b32 v61, v61, s69, v154
	v_bfe_u32 v60, v60, 16, 16
	v_lshl_or_b32 v60, v60, 10, v154
	global_load_lds_dwordx4 v61, s[28:29]
	s_mov_b32 m0, s56
	s_nop 0
	global_load_lds_dwordx4 v60, s[28:29]
	s_waitcnt vmcnt(8)
	s_waitcnt lgkmcnt(0)
	s_barrier
	v_mfma_f32_16x16x128_f8f6f4 v[132:135], v[136:143], v[68:75], v[132:135]
	v_mfma_f32_16x16x128_f8f6f4 v[124:127], v[156:163], v[68:75], v[124:127]
	v_mfma_f32_16x16x128_f8f6f4 v[116:119], v[136:143], v[194:201], v[116:119]
	v_mfma_f32_16x16x128_f8f6f4 v[108:111], v[156:163], v[194:201], v[108:111]
	v_mfma_f32_16x16x128_f8f6f4 v[100:103], v[136:143], v[228:235], v[144:147]
	v_mfma_f32_16x16x128_f8f6f4 v[92:95], v[156:163], v[228:235], v[180:183]
	v_mfma_f32_16x16x128_f8f6f4 v[84:87], v[136:143], v[236:243], v[186:189]
	v_mfma_f32_16x16x128_f8f6f4 v[76:79], v[156:163], v[236:243], v[190:193]
	v_mfma_f32_16x16x128_f8f6f4 v[128:131], v[164:171], v[68:75], v[128:131]
	v_mfma_f32_16x16x128_f8f6f4 v[120:123], v[172:179], v[68:75], v[120:123]
	v_mfma_f32_16x16x128_f8f6f4 v[112:115], v[164:171], v[194:201], v[112:115]
	v_mfma_f32_16x16x128_f8f6f4 v[104:107], v[172:179], v[194:201], v[104:107]
	v_mfma_f32_16x16x128_f8f6f4 v[96:99], v[164:171], v[228:235], v[202:205]
	v_mfma_f32_16x16x128_f8f6f4 v[88:91], v[172:179], v[228:235], v[206:209]
	v_mfma_f32_16x16x128_f8f6f4 v[80:83], v[164:171], v[236:243], v[210:213]
	v_mfma_f32_16x16x128_f8f6f4 v[72:75], v[172:179], v[236:243], v[214:217]
	s_barrier
	v_mov_b32_e32 v184, v152
	ds_read_b128 v[194:197], v148 offset:49152
	ds_read_b128 v[228:231], v148 offset:51200
	ds_read_b128 v[198:201], v149 offset:49152
	ds_read_b128 v[232:235], v149 offset:51200
	ds_read_b128 v[236:239], v148 offset:53248
	ds_read_b128 v[244:247], v148 offset:55296
	ds_read_b128 v[240:243], v149 offset:53248
	ds_read_b128 v[248:251], v149 offset:55296
	s_mov_b32 m0, s57
	v_lshl_add_u64 v[60:61], s[36:37], 0, v[184:185]
	v_lshl_add_u64 v[60:61], v[60:61], 0, s[46:47]
	v_mov_b32_e32 v184, v153
	global_load_lds_dwordx4 v[60:61], off
	s_mov_b32 m0, s59
	v_lshl_add_u64 v[60:61], s[36:37], 0, v[184:185]
	v_lshl_add_u64 v[60:61], v[60:61], 0, s[46:47]
	global_load_lds_dwordx4 v[60:61], off
	s_add_u32 s36, s36, 0x20080
	v_mov_b32_e32 v60, v152
	s_addc_u32 s37, s37, 0
	s_mov_b32 m0, s66
	s_nop 0
	global_load_lds_dwordx4 v60, s[36:37]
	v_mov_b32_e32 v60, v153
	s_mov_b32 m0, s67
	s_nop 0
	global_load_lds_dwordx4 v60, s[36:37]
	v_mbcnt_lo_u32_b32 v60, -1, 0
	v_mbcnt_hi_u32_b32 v60, -1, v60
	s_mov_b32 s36, s61
	v_lshlrev_b32_e32 v60, 3, v60
	s_mov_b32 m0, s64
	v_lshl_or_b32 v60, s36, 9, v60
	v_add_u32_e32 v60, s78, v60
	ds_read_b32 v62, v60
	s_waitcnt lgkmcnt(0)
	v_lshlrev_b32_e32 v60, 10, v62
	v_and_or_b32 v184, v60, s69, v154
	s_nop 0
	v_lshl_add_u64 v[60:61], s[28:29], 0, v[184:185]
	v_lshl_add_u64 v[60:61], v[60:61], 0, s[46:47]
	global_load_lds_dwordx4 v[60:61], off
	v_bfe_u32 v60, v62, 16, 16
	v_lshl_or_b32 v184, v60, 10, v154
	s_mov_b32 m0, s65
	v_lshl_add_u64 v[60:61], s[28:29], 0, v[184:185]
	v_lshl_add_u64 v[60:61], v[60:61], 0, s[46:47]
	global_load_lds_dwordx4 v[60:61], off
	s_waitcnt vmcnt(8)
	s_waitcnt lgkmcnt(0)
	s_barrier
	v_mfma_f32_16x16x128_f8f6f4 v[68:71], v[136:143], v[194:201], v[40:43]
	v_mfma_f32_16x16x128_f8f6f4 v[60:63], v[156:163], v[194:201], v[52:55]
	v_mfma_f32_16x16x128_f8f6f4 v[48:51], v[136:143], v[228:235], v[48:51]
	v_mfma_f32_16x16x128_f8f6f4 v[36:39], v[156:163], v[228:235], v[36:39]
	v_mfma_f32_16x16x128_f8f6f4 v[28:31], v[136:143], v[236:243], v[28:31]
	v_mfma_f32_16x16x128_f8f6f4 v[20:23], v[156:163], v[236:243], v[20:23]
	v_mfma_f32_16x16x128_f8f6f4 v[12:15], v[136:143], v[244:251], v[12:15]
	v_mfma_f32_16x16x128_f8f6f4 v[4:7], v[156:163], v[244:251], v[4:7]
	v_mfma_f32_16x16x128_f8f6f4 v[64:67], v[164:171], v[194:201], v[64:67]
	v_mfma_f32_16x16x128_f8f6f4 v[56:59], v[172:179], v[194:201], v[56:59]
	v_mfma_f32_16x16x128_f8f6f4 v[44:47], v[164:171], v[228:235], v[44:47]
	v_mfma_f32_16x16x128_f8f6f4 v[32:35], v[172:179], v[228:235], v[32:35]
	v_mfma_f32_16x16x128_f8f6f4 v[24:27], v[164:171], v[236:243], v[24:27]
	v_mfma_f32_16x16x128_f8f6f4 v[16:19], v[172:179], v[236:243], v[16:19]
	v_mfma_f32_16x16x128_f8f6f4 v[8:11], v[164:171], v[244:251], v[8:11]
	v_mfma_f32_16x16x128_f8f6f4 v[0:3], v[172:179], v[244:251], v[0:3]
	s_barrier
	s_add_i32 s77, s77, 2
	s_add_u32 s24, s24, 0x100
	s_addc_u32 s25, s25, 0
	s_add_u32 s19, s19, 0x100
	s_addc_u32 s76, s76, 0
.LBB0_1035:
	ds_read_b128 v[136:139], v150
	ds_read_b128 v[156:159], v150 offset:2048
	ds_read_b128 v[140:143], v151
	ds_read_b128 v[160:163], v151 offset:2048
	ds_read_b128 v[164:167], v150 offset:16384
	ds_read_b128 v[172:175], v150 offset:18432
	ds_read_b128 v[168:171], v151 offset:16384
	ds_read_b128 v[176:179], v151 offset:18432
	s_add_u32 s28, s24, 0x80
	s_addc_u32 s29, s25, 0
	s_cmp_eq_u32 s77, 4
	s_cselect_b32 s29, s11, s29
	s_cselect_b32 s28, s10, s28
	s_cselect_b32 s80, s27, s75
	s_cselect_b32 s37, s23, s76
	s_cselect_b32 s36, s22, s19
	ds_read_b128 v[194:197], v148
	ds_read_b128 v[228:231], v148 offset:2048
	ds_read_b128 v[198:201], v149
	ds_read_b128 v[232:235], v149 offset:2048
	ds_read_b128 v[236:239], v148 offset:4096
	ds_read_b128 v[244:247], v148 offset:6144
	ds_read_b128 v[240:243], v149 offset:4096
	ds_read_b128 v[248:251], v149 offset:6144
	v_mbcnt_lo_u32_b32 v40, -1, 0
	v_mbcnt_hi_u32_b32 v40, -1, v40
	s_mov_b32 s78, s61
	v_lshlrev_b32_e32 v40, 3, v40
	s_add_i32 m0, s35, 0xc000
	v_lshl_or_b32 v40, s78, 9, v40
	v_add_u32_e32 v40, s74, v40
	ds_read_b32 v40, v40 offset:4
	s_waitcnt lgkmcnt(0)
	v_lshlrev_b32_e32 v41, 10, v40
	v_and_or_b32 v41, v41, s69, v154
	v_bfe_u32 v40, v40, 16, 16
	v_lshl_or_b32 v40, v40, 10, v154
	global_load_lds_dwordx4 v41, s[24:25]
	s_add_i32 m0, s35, 0xe000
	s_nop 0
	global_load_lds_dwordx4 v40, s[24:25]
	s_waitcnt vmcnt(8)
	s_waitcnt lgkmcnt(0)
	s_barrier
	v_mfma_f32_16x16x128_f8f6f4 v[132:135], v[136:143], v[194:201], v[132:135]
	v_mfma_f32_16x16x128_f8f6f4 v[124:127], v[156:163], v[194:201], v[124:127]
	v_mfma_f32_16x16x128_f8f6f4 v[116:119], v[136:143], v[228:235], v[116:119]
	v_mfma_f32_16x16x128_f8f6f4 v[108:111], v[156:163], v[228:235], v[108:111]
	v_mfma_f32_16x16x128_f8f6f4 v[144:147], v[136:143], v[236:243], v[100:103]
	v_mfma_f32_16x16x128_f8f6f4 v[180:183], v[156:163], v[236:243], v[92:95]
	v_mfma_f32_16x16x128_f8f6f4 v[186:189], v[136:143], v[244:251], v[84:87]
	v_mfma_f32_16x16x128_f8f6f4 v[190:193], v[156:163], v[244:251], v[76:79]
	v_mfma_f32_16x16x128_f8f6f4 v[128:131], v[164:171], v[194:201], v[128:131]
	v_mfma_f32_16x16x128_f8f6f4 v[120:123], v[172:179], v[194:201], v[120:123]
	v_mfma_f32_16x16x128_f8f6f4 v[112:115], v[164:171], v[228:235], v[112:115]
	v_mfma_f32_16x16x128_f8f6f4 v[104:107], v[172:179], v[228:235], v[104:107]
	v_mfma_f32_16x16x128_f8f6f4 v[202:205], v[164:171], v[236:243], v[96:99]
	v_mfma_f32_16x16x128_f8f6f4 v[206:209], v[172:179], v[236:243], v[88:91]
	v_mfma_f32_16x16x128_f8f6f4 v[210:213], v[164:171], v[244:251], v[80:83]
	v_mfma_f32_16x16x128_f8f6f4 v[214:217], v[172:179], v[244:251], v[72:75]
	s_barrier
	v_mov_b32_e32 v40, v152
	s_mov_b32 m0, s44
	s_nop 2
	ds_read_b128 v[72:75], v148 offset:16384
	ds_read_b128 v[80:83], v148 offset:18432
	ds_read_b128 v[76:79], v149 offset:16384
	ds_read_b128 v[84:87], v149 offset:18432
	ds_read_b128 v[88:91], v148 offset:20480
	ds_read_b128 v[96:99], v148 offset:22528
	ds_read_b128 v[92:95], v149 offset:20480
	ds_read_b128 v[100:103], v149 offset:22528
	s_add_u32 s78, s36, 0x20000
	global_load_lds_dwordx4 v40, s[36:37]
	v_mov_b32_e32 v40, v153
	s_mov_b32 m0, s49
	s_addc_u32 s79, s37, 0
	global_load_lds_dwordx4 v40, s[36:37]
	v_mov_b32_e32 v40, v152
	s_mov_b32 m0, s50
	s_nop 0
	global_load_lds_dwordx4 v40, s[78:79]
	v_mov_b32_e32 v40, v153
	s_mov_b32 m0, s51
	s_nop 0
	global_load_lds_dwordx4 v40, s[78:79]
	v_mbcnt_lo_u32_b32 v40, -1, 0
	v_mbcnt_hi_u32_b32 v40, -1, v40
	s_mov_b32 s78, s61
	v_lshlrev_b32_e32 v40, 3, v40
	v_lshl_or_b32 v40, s78, 9, v40
	s_lshl_b32 s78, s80, 12
	s_add_i32 s78, s78, 0
	s_add_i32 s78, s78, 0x21000
	v_add_u32_e32 v40, s78, v40
	ds_read_b32 v40, v40
	s_mov_b32 m0, s35
	s_waitcnt lgkmcnt(0)
	v_lshlrev_b32_e32 v41, 10, v40
	v_and_or_b32 v41, v41, s69, v154
	v_bfe_u32 v40, v40, 16, 16
	v_lshl_or_b32 v40, v40, 10, v154
	global_load_lds_dwordx4 v41, s[28:29]
	s_mov_b32 m0, s54
	s_nop 0
	global_load_lds_dwordx4 v40, s[28:29]
	s_waitcnt vmcnt(8)
	s_waitcnt lgkmcnt(0)
	s_barrier
	v_mfma_f32_16x16x128_f8f6f4 v[48:51], v[136:143], v[80:87], v[48:51]
	v_mfma_f32_16x16x128_f8f6f4 v[36:39], v[156:163], v[80:87], v[36:39]
	v_mfma_f32_16x16x128_f8f6f4 v[28:31], v[136:143], v[88:95], v[28:31]
	v_mfma_f32_16x16x128_f8f6f4 v[20:23], v[156:163], v[88:95], v[20:23]
	v_mfma_f32_16x16x128_f8f6f4 v[12:15], v[136:143], v[96:103], v[12:15]
	v_mfma_f32_16x16x128_f8f6f4 v[4:7], v[156:163], v[96:103], v[4:7]
	v_mfma_f32_16x16x128_f8f6f4 v[40:43], v[136:143], v[72:79], v[68:71]
	v_mfma_f32_16x16x128_f8f6f4 v[52:55], v[156:163], v[72:79], v[60:63]
	v_mfma_f32_16x16x128_f8f6f4 v[64:67], v[164:171], v[72:79], v[64:67]
	v_mfma_f32_16x16x128_f8f6f4 v[56:59], v[172:179], v[72:79], v[56:59]
	v_mfma_f32_16x16x128_f8f6f4 v[44:47], v[164:171], v[80:87], v[44:47]
	v_mfma_f32_16x16x128_f8f6f4 v[32:35], v[172:179], v[80:87], v[32:35]
	v_mfma_f32_16x16x128_f8f6f4 v[24:27], v[164:171], v[88:95], v[24:27]
	v_mfma_f32_16x16x128_f8f6f4 v[16:19], v[172:179], v[88:95], v[16:19]
	v_mfma_f32_16x16x128_f8f6f4 v[8:11], v[164:171], v[96:103], v[8:11]
	v_mfma_f32_16x16x128_f8f6f4 v[0:3], v[172:179], v[96:103], v[0:3]
	s_barrier
	ds_read_b128 v[136:139], v150 offset:32768
	ds_read_b128 v[156:159], v150 offset:34816
	ds_read_b128 v[140:143], v151 offset:32768
	ds_read_b128 v[160:163], v151 offset:34816
	ds_read_b128 v[164:167], v150 offset:49152
	ds_read_b128 v[172:175], v150 offset:51200
	ds_read_b128 v[168:171], v151 offset:49152
	ds_read_b128 v[176:179], v151 offset:51200
	ds_read_b128 v[68:71], v148 offset:32768
	ds_read_b128 v[194:197], v148 offset:34816
	ds_read_b128 v[72:75], v149 offset:32768
	ds_read_b128 v[198:201], v149 offset:34816
	ds_read_b128 v[228:231], v148 offset:36864
	ds_read_b128 v[236:239], v148 offset:38912
	ds_read_b128 v[232:235], v149 offset:36864
	ds_read_b128 v[240:243], v149 offset:38912
	v_mbcnt_lo_u32_b32 v60, -1, 0
	v_mbcnt_hi_u32_b32 v60, -1, v60
	s_mov_b32 s79, s61
	v_lshlrev_b32_e32 v60, 3, v60
	s_mov_b32 m0, s55
	v_lshl_or_b32 v60, s79, 9, v60
	v_add_u32_e32 v60, s78, v60
	ds_read_b32 v60, v60 offset:4
	s_waitcnt lgkmcnt(0)
	v_lshlrev_b32_e32 v61, 10, v60
	v_and_or_b32 v61, v61, s69, v154
	v_bfe_u32 v60, v60, 16, 16
	v_lshl_or_b32 v60, v60, 10, v154
	global_load_lds_dwordx4 v61, s[28:29]
	s_mov_b32 m0, s56
	s_nop 0
	global_load_lds_dwordx4 v60, s[28:29]
	s_waitcnt vmcnt(8)
	s_waitcnt lgkmcnt(0)
	s_barrier
	v_mfma_f32_16x16x128_f8f6f4 v[132:135], v[136:143], v[68:75], v[132:135]
	v_mfma_f32_16x16x128_f8f6f4 v[124:127], v[156:163], v[68:75], v[124:127]
	v_mfma_f32_16x16x128_f8f6f4 v[116:119], v[136:143], v[194:201], v[116:119]
	v_mfma_f32_16x16x128_f8f6f4 v[108:111], v[156:163], v[194:201], v[108:111]
	v_mfma_f32_16x16x128_f8f6f4 v[100:103], v[136:143], v[228:235], v[144:147]
	v_mfma_f32_16x16x128_f8f6f4 v[92:95], v[156:163], v[228:235], v[180:183]
	v_mfma_f32_16x16x128_f8f6f4 v[84:87], v[136:143], v[236:243], v[186:189]
	v_mfma_f32_16x16x128_f8f6f4 v[76:79], v[156:163], v[236:243], v[190:193]
	v_mfma_f32_16x16x128_f8f6f4 v[128:131], v[164:171], v[68:75], v[128:131]
	v_mfma_f32_16x16x128_f8f6f4 v[120:123], v[172:179], v[68:75], v[120:123]
	v_mfma_f32_16x16x128_f8f6f4 v[112:115], v[164:171], v[194:201], v[112:115]
	v_mfma_f32_16x16x128_f8f6f4 v[104:107], v[172:179], v[194:201], v[104:107]
	v_mfma_f32_16x16x128_f8f6f4 v[96:99], v[164:171], v[228:235], v[202:205]
	v_mfma_f32_16x16x128_f8f6f4 v[88:91], v[172:179], v[228:235], v[206:209]
	v_mfma_f32_16x16x128_f8f6f4 v[80:83], v[164:171], v[236:243], v[210:213]
	v_mfma_f32_16x16x128_f8f6f4 v[72:75], v[172:179], v[236:243], v[214:217]
	s_barrier
	v_mov_b32_e32 v184, v152
	ds_read_b128 v[194:197], v148 offset:49152
	ds_read_b128 v[228:231], v148 offset:51200
	ds_read_b128 v[198:201], v149 offset:49152
	ds_read_b128 v[232:235], v149 offset:51200
	ds_read_b128 v[236:239], v148 offset:53248
	ds_read_b128 v[244:247], v148 offset:55296
	ds_read_b128 v[240:243], v149 offset:53248
	ds_read_b128 v[248:251], v149 offset:55296
	s_mov_b32 m0, s57
	v_lshl_add_u64 v[60:61], s[36:37], 0, v[184:185]
	v_lshl_add_u64 v[60:61], v[60:61], 0, s[46:47]
	v_mov_b32_e32 v184, v153
	global_load_lds_dwordx4 v[60:61], off
	s_mov_b32 m0, s59
	v_lshl_add_u64 v[60:61], s[36:37], 0, v[184:185]
	v_lshl_add_u64 v[60:61], v[60:61], 0, s[46:47]
	global_load_lds_dwordx4 v[60:61], off
	s_add_u32 s36, s36, 0x20080
	v_mov_b32_e32 v60, v152
	s_addc_u32 s37, s37, 0
	s_mov_b32 m0, s66
	s_nop 0
	global_load_lds_dwordx4 v60, s[36:37]
	v_mov_b32_e32 v60, v153
	s_mov_b32 m0, s67
	s_nop 0
	global_load_lds_dwordx4 v60, s[36:37]
	v_mbcnt_lo_u32_b32 v60, -1, 0
	v_mbcnt_hi_u32_b32 v60, -1, v60
	s_mov_b32 s36, s61
	v_lshlrev_b32_e32 v60, 3, v60
	s_mov_b32 m0, s64
	v_lshl_or_b32 v60, s36, 9, v60
	v_add_u32_e32 v60, s78, v60
	ds_read_b32 v62, v60
	s_waitcnt lgkmcnt(0)
	v_lshlrev_b32_e32 v60, 10, v62
	v_and_or_b32 v184, v60, s69, v154
	s_nop 0
	v_lshl_add_u64 v[60:61], s[28:29], 0, v[184:185]
	v_lshl_add_u64 v[60:61], v[60:61], 0, s[46:47]
	global_load_lds_dwordx4 v[60:61], off
	v_bfe_u32 v60, v62, 16, 16
	v_lshl_or_b32 v184, v60, 10, v154
	s_mov_b32 m0, s65
	v_lshl_add_u64 v[60:61], s[28:29], 0, v[184:185]
	v_lshl_add_u64 v[60:61], v[60:61], 0, s[46:47]
	global_load_lds_dwordx4 v[60:61], off
	s_waitcnt vmcnt(8)
	s_waitcnt lgkmcnt(0)
	s_barrier
	v_mfma_f32_16x16x128_f8f6f4 v[68:71], v[136:143], v[194:201], v[40:43]
	v_mfma_f32_16x16x128_f8f6f4 v[60:63], v[156:163], v[194:201], v[52:55]
	v_mfma_f32_16x16x128_f8f6f4 v[48:51], v[136:143], v[228:235], v[48:51]
	v_mfma_f32_16x16x128_f8f6f4 v[36:39], v[156:163], v[228:235], v[36:39]
	v_mfma_f32_16x16x128_f8f6f4 v[28:31], v[136:143], v[236:243], v[28:31]
	v_mfma_f32_16x16x128_f8f6f4 v[20:23], v[156:163], v[236:243], v[20:23]
	v_mfma_f32_16x16x128_f8f6f4 v[12:15], v[136:143], v[244:251], v[12:15]
	v_mfma_f32_16x16x128_f8f6f4 v[4:7], v[156:163], v[244:251], v[4:7]
	v_mfma_f32_16x16x128_f8f6f4 v[64:67], v[164:171], v[194:201], v[64:67]
	v_mfma_f32_16x16x128_f8f6f4 v[56:59], v[172:179], v[194:201], v[56:59]
	v_mfma_f32_16x16x128_f8f6f4 v[44:47], v[164:171], v[228:235], v[44:47]
	v_mfma_f32_16x16x128_f8f6f4 v[32:35], v[172:179], v[228:235], v[32:35]
	v_mfma_f32_16x16x128_f8f6f4 v[24:27], v[164:171], v[236:243], v[24:27]
	v_mfma_f32_16x16x128_f8f6f4 v[16:19], v[172:179], v[236:243], v[16:19]
	v_mfma_f32_16x16x128_f8f6f4 v[8:11], v[164:171], v[244:251], v[8:11]
	v_mfma_f32_16x16x128_f8f6f4 v[0:3], v[172:179], v[244:251], v[0:3]
	s_barrier
	s_add_i32 s77, s77, 2
	s_add_u32 s24, s24, 0x100
	s_addc_u32 s25, s25, 0
	s_add_u32 s19, s19, 0x100
	s_addc_u32 s76, s76, 0
	s_cmp_gt_u32 s77, 5
	s_cbranch_scc0 .LBB0_1035
	s_and_b64 vcc, exec, s[8:9]
	s_mov_b32 s36, s26
	s_mov_b32 s28, s73
	s_mov_b64 s[8:9], 0
	s_cbranch_vccz .LBB0_1039
	s_add_i32 s8, s72, 2
	s_mul_i32 s9, s8, s31
	s_mul_hi_u32 s19, s8, s0
	s_add_i32 s19, s19, s9
	s_mul_i32 s8, s8, s0
	s_add_u32 s24, s8, s1
	s_addc_u32 s25, s19, s40
	v_mov_b64_e32 v[40:41], s[4:5]
	v_cmp_ge_i64_e32 vcc, s[24:25], v[40:41]
	s_mov_b64 s[8:9], 0
	s_mov_b32 s28, s73
	s_mov_b32 s36, s26
	s_cbranch_vccnz .LBB0_1039
	s_ashr_i32 s8, s24, 31
	s_lshr_b32 s8, s8, 29
	s_add_i32 s8, s24, s8
	s_ashr_i32 s9, s8, 3
	s_and_b32 s8, s8, -8
	s_sub_i32 s8, s24, s8
	s_lshr_b32 s19, s8, 31
	s_add_i32 s19, s33, s19
	s_mul_i32 s8, s19, s8
	s_add_i32 s8, s8, s9
	s_ashr_i32 s9, s8, 31
	s_lshr_b32 s9, s9, 26
	s_add_i32 s9, s8, s9
	s_ashr_i32 s19, s9, 6
	s_lshl_b32 s19, s19, 3
	s_sub_i32 s24, s33, s19
	s_min_i32 s24, s24, 8
	s_abs_i32 s25, s24
	v_cvt_f32_u32_e32 v40, s25
	s_sub_i32 s29, 0, s25
	s_andn2_b32 s9, s9, 63
	s_sub_i32 s8, s8, s9
	v_rcp_iflag_f32_e32 v40, v40
	s_abs_i32 s9, s8
	s_xor_b32 s28, s8, s24
	s_ashr_i32 s28, s28, 31
	v_mul_f32_e32 v40, 0x4f7ffffe, v40
	v_cvt_u32_f32_e32 v40, v40
	s_nop 0
	v_readfirstlane_b32 s36, v40
	s_mul_i32 s29, s29, s36
	s_mul_hi_u32 s29, s36, s29
	s_add_i32 s36, s36, s29
	s_mul_hi_u32 s29, s9, s36
	s_mul_i32 s36, s29, s25
	s_sub_i32 s9, s9, s36
	s_add_i32 s37, s29, 1
	s_sub_i32 s36, s9, s25
	s_cmp_ge_u32 s9, s25
	s_cselect_b32 s29, s37, s29
	s_cselect_b32 s9, s36, s9
	s_add_i32 s36, s29, 1
	s_cmp_ge_u32 s9, s25
	s_cselect_b32 s9, s36, s29
	s_xor_b32 s9, s9, s28
	s_sub_i32 s36, s9, s28
	s_mul_i32 s9, s36, s24
	s_sub_i32 s8, s8, s9
	s_add_i32 s28, s8, s19
	s_mov_b64 s[8:9], -1

.LBB0_1113:
	s_ashr_i32 s25, s24, 31
	s_lshl_b64 s[22:23], s[24:25], 18
	s_add_u32 s22, s38, s22
	s_addc_u32 s23, s39, s23
	s_and_b64 s[34:35], s[10:11], exec
	s_cselect_b32 s7, s23, s29
	s_cselect_b32 s21, s22, s28
	s_add_u32 s28, s28, 0x20080
	s_addc_u32 s29, s29, 0
	s_add_u32 s25, s30, 0x100
	s_addc_u32 s80, s31, 0
	s_mov_b32 s81, -2
	ds_read_b128 v[128:131], v148
	ds_read_b128 v[136:139], v148 offset:2048
	ds_read_b128 v[132:135], v149
	ds_read_b128 v[140:143], v149 offset:2048
	ds_read_b128 v[152:155], v148 offset:16384
	ds_read_b128 v[160:163], v148 offset:18432
	ds_read_b128 v[156:159], v149 offset:16384
	ds_read_b128 v[164:167], v149 offset:18432
	s_add_u32 s30, s28, 0xfffe0080
	s_addc_u32 s31, s29, -1
	s_cmp_eq_u32 s81, 4
	s_cselect_b32 s31, s7, s31
	s_cselect_b32 s30, s21, s30
	s_cselect_b32 s35, s19, s80
	s_cselect_b32 s34, s18, s25
	v_mov_b32_e32 v144, v150
	ds_read_b128 v[168:171], v146
	ds_read_b128 v[176:179], v146 offset:2048
	ds_read_b128 v[172:175], v147
	ds_read_b128 v[180:183], v147 offset:2048
	ds_read_b128 v[194:197], v146 offset:4096
	ds_read_b128 v[228:231], v146 offset:6144
	ds_read_b128 v[198:201], v147 offset:4096
	ds_read_b128 v[232:235], v147 offset:6144
	s_add_i32 m0, s27, 0xc000
	s_nop 0
	global_load_lds_dwordx4 v144, s[28:29]
	v_mov_b32_e32 v144, v151
	s_add_i32 m0, s27, 0xe000
	s_nop 0
	global_load_lds_dwordx4 v144, s[28:29]
	s_waitcnt vmcnt(8)
	s_waitcnt lgkmcnt(0)
	s_barrier
	v_mfma_f32_16x16x128_f8f6f4 v[124:127], v[128:135], v[168:175], 0
	v_mfma_f32_16x16x128_f8f6f4 v[120:123], v[136:143], v[168:175], 0
	v_mfma_f32_16x16x128_f8f6f4 v[108:111], v[128:135], v[176:183], 0
	v_mfma_f32_16x16x128_f8f6f4 v[104:107], v[136:143], v[176:183], 0
	v_mfma_f32_16x16x128_f8f6f4 v[186:189], v[128:135], v[194:201], 0
	v_mfma_f32_16x16x128_f8f6f4 v[190:193], v[136:143], v[194:201], 0
	v_mfma_f32_16x16x128_f8f6f4 v[202:205], v[128:135], v[228:235], 0
	v_mfma_f32_16x16x128_f8f6f4 v[206:209], v[136:143], v[228:235], 0
	v_mfma_f32_16x16x128_f8f6f4 v[116:119], v[152:159], v[168:175], 0
	v_mfma_f32_16x16x128_f8f6f4 v[112:115], v[160:167], v[168:175], 0
	v_mfma_f32_16x16x128_f8f6f4 v[100:103], v[152:159], v[176:183], 0
	v_mfma_f32_16x16x128_f8f6f4 v[96:99], v[160:167], v[176:183], 0
	v_mfma_f32_16x16x128_f8f6f4 v[168:171], v[152:159], v[194:201], 0
	v_mfma_f32_16x16x128_f8f6f4 v[172:175], v[160:167], v[194:201], 0
	v_mfma_f32_16x16x128_f8f6f4 v[176:179], v[152:159], v[228:235], 0
	v_mfma_f32_16x16x128_f8f6f4 v[180:183], v[160:167], v[228:235], 0
	s_barrier
	v_mov_b32_e32 v144, v150
	s_mov_b32 m0, s43
	s_nop 2
	ds_read_b128 v[64:67], v146 offset:16384
	ds_read_b128 v[72:75], v146 offset:18432
	ds_read_b128 v[68:71], v147 offset:16384
	ds_read_b128 v[76:79], v147 offset:18432
	ds_read_b128 v[80:83], v146 offset:20480
	ds_read_b128 v[88:91], v146 offset:22528
	ds_read_b128 v[84:87], v147 offset:20480
	ds_read_b128 v[92:95], v147 offset:22528
	s_add_u32 s82, s34, 0x20000
	global_load_lds_dwordx4 v144, s[34:35]
	v_mov_b32_e32 v144, v151
	s_mov_b32 m0, s44
	s_addc_u32 s83, s35, 0
	global_load_lds_dwordx4 v144, s[34:35]
	v_mov_b32_e32 v144, v150
	s_mov_b32 m0, s49
	s_nop 0
	global_load_lds_dwordx4 v144, s[82:83]
	v_mov_b32_e32 v144, v151
	s_mov_b32 m0, s50
	s_nop 0
	global_load_lds_dwordx4 v144, s[82:83]
	v_mov_b32_e32 v144, v150
	s_mov_b32 m0, s27
	s_nop 0
	global_load_lds_dwordx4 v144, s[30:31]
	v_mov_b32_e32 v144, v151
	s_mov_b32 m0, s51
	s_nop 0
	global_load_lds_dwordx4 v144, s[30:31]
	s_waitcnt vmcnt(8)
	s_waitcnt lgkmcnt(0)
	s_barrier
	v_mfma_f32_16x16x128_f8f6f4 v[60:63], v[128:135], v[64:71], 0
	v_mfma_f32_16x16x128_f8f6f4 v[56:59], v[136:143], v[64:71], 0
	v_mfma_f32_16x16x128_f8f6f4 v[194:197], v[128:135], v[72:79], 0
	v_mfma_f32_16x16x128_f8f6f4 v[198:201], v[136:143], v[72:79], 0
	v_mfma_f32_16x16x128_f8f6f4 v[210:213], v[128:135], v[80:87], 0
	v_mfma_f32_16x16x128_f8f6f4 v[214:217], v[136:143], v[80:87], 0
	v_mfma_f32_16x16x128_f8f6f4 v[218:221], v[128:135], v[88:95], 0
	v_mfma_f32_16x16x128_f8f6f4 v[222:225], v[136:143], v[88:95], 0
	v_mfma_f32_16x16x128_f8f6f4 v[52:55], v[152:159], v[64:71], 0
	v_mfma_f32_16x16x128_f8f6f4 v[48:51], v[160:167], v[64:71], 0
	v_mfma_f32_16x16x128_f8f6f4 v[228:231], v[152:159], v[72:79], 0
	v_mfma_f32_16x16x128_f8f6f4 v[232:235], v[160:167], v[72:79], 0
	v_mfma_f32_16x16x128_f8f6f4 v[236:239], v[152:159], v[80:87], 0
	v_mfma_f32_16x16x128_f8f6f4 v[240:243], v[160:167], v[80:87], 0
	v_mfma_f32_16x16x128_f8f6f4 v[244:247], v[152:159], v[88:95], 0
	v_mfma_f32_16x16x128_f8f6f4 v[248:251], v[160:167], v[88:95], 0
	s_barrier
	s_nop 4
	ds_read_b128 v[0:3], v148 offset:32768
	ds_read_b128 v[16:19], v148 offset:34816
	ds_read_b128 v[4:7], v149 offset:32768
	ds_read_b128 v[20:23], v149 offset:34816
	ds_read_b128 v[128:131], v148 offset:49152
	ds_read_b128 v[136:139], v148 offset:51200
	ds_read_b128 v[132:135], v149 offset:49152
	ds_read_b128 v[140:143], v149 offset:51200
	s_add_u32 s82, s30, 0x20000
	v_mov_b32_e32 v64, v150
	s_mov_b32 m0, s54
	ds_read_b128 v[8:11], v146 offset:32768
	ds_read_b128 v[24:27], v146 offset:34816
	ds_read_b128 v[12:15], v147 offset:32768
	ds_read_b128 v[28:31], v147 offset:34816
	ds_read_b128 v[32:35], v146 offset:36864
	ds_read_b128 v[40:43], v146 offset:38912
	ds_read_b128 v[36:39], v147 offset:36864
	ds_read_b128 v[44:47], v147 offset:38912
	s_addc_u32 s83, s31, 0
	s_nop 0
	global_load_lds_dwordx4 v64, s[82:83]
	v_mov_b32_e32 v64, v151
	s_mov_b32 m0, s55
	s_nop 0
	global_load_lds_dwordx4 v64, s[82:83]
	s_waitcnt vmcnt(8)
	s_waitcnt lgkmcnt(0)
	s_barrier
	v_mfma_f32_16x16x128_f8f6f4 v[124:127], v[0:7], v[8:15], v[124:127]
	v_mfma_f32_16x16x128_f8f6f4 v[120:123], v[16:23], v[8:15], v[120:123]
	v_mfma_f32_16x16x128_f8f6f4 v[108:111], v[0:7], v[24:31], v[108:111]
	v_mfma_f32_16x16x128_f8f6f4 v[104:107], v[16:23], v[24:31], v[104:107]
	v_mfma_f32_16x16x128_f8f6f4 v[92:95], v[0:7], v[32:39], v[186:189]
	v_mfma_f32_16x16x128_f8f6f4 v[88:91], v[16:23], v[32:39], v[190:193]
	v_mfma_f32_16x16x128_f8f6f4 v[76:79], v[0:7], v[40:47], v[202:205]
	v_mfma_f32_16x16x128_f8f6f4 v[72:75], v[16:23], v[40:47], v[206:209]
	v_mfma_f32_16x16x128_f8f6f4 v[116:119], v[128:135], v[8:15], v[116:119]
	v_mfma_f32_16x16x128_f8f6f4 v[112:115], v[136:143], v[8:15], v[112:115]
	v_mfma_f32_16x16x128_f8f6f4 v[100:103], v[128:135], v[24:31], v[100:103]
	v_mfma_f32_16x16x128_f8f6f4 v[96:99], v[136:143], v[24:31], v[96:99]
	v_mfma_f32_16x16x128_f8f6f4 v[84:87], v[128:135], v[32:39], v[168:171]
	v_mfma_f32_16x16x128_f8f6f4 v[80:83], v[136:143], v[32:39], v[172:175]
	v_mfma_f32_16x16x128_f8f6f4 v[68:71], v[128:135], v[40:47], v[176:179]
	v_mfma_f32_16x16x128_f8f6f4 v[64:67], v[136:143], v[40:47], v[180:183]
	s_barrier
	v_mov_b32_e32 v184, v150
	ds_read_b128 v[32:35], v146 offset:49152
	ds_read_b128 v[152:155], v146 offset:51200
	ds_read_b128 v[36:39], v147 offset:49152
	ds_read_b128 v[156:159], v147 offset:51200
	ds_read_b128 v[160:163], v146 offset:53248
	ds_read_b128 v[168:171], v146 offset:55296
	ds_read_b128 v[164:167], v147 offset:53248
	ds_read_b128 v[172:175], v147 offset:55296
	s_mov_b32 m0, s56
	v_lshl_add_u64 v[8:9], s[34:35], 0, v[184:185]
	v_lshl_add_u64 v[8:9], v[8:9], 0, s[46:47]
	v_mov_b32_e32 v184, v151
	global_load_lds_dwordx4 v[8:9], off
	s_mov_b32 m0, s57
	v_lshl_add_u64 v[8:9], s[34:35], 0, v[184:185]
	v_lshl_add_u64 v[8:9], v[8:9], 0, s[46:47]
	global_load_lds_dwordx4 v[8:9], off
	s_add_u32 s34, s34, 0x20080
	v_mov_b32_e32 v8, v150
	s_addc_u32 s35, s35, 0
	s_mov_b32 m0, s65
	v_mov_b32_e32 v184, v150
	global_load_lds_dwordx4 v8, s[34:35]
	v_mov_b32_e32 v8, v151
	s_mov_b32 m0, s66
	s_nop 0
	global_load_lds_dwordx4 v8, s[34:35]
	s_mov_b32 m0, s59
	v_lshl_add_u64 v[8:9], s[30:31], 0, v[184:185]
	v_lshl_add_u64 v[8:9], v[8:9], 0, s[46:47]
	v_mov_b32_e32 v184, v151
	global_load_lds_dwordx4 v[8:9], off
	s_mov_b32 m0, s64
	v_lshl_add_u64 v[8:9], s[30:31], 0, v[184:185]
	v_lshl_add_u64 v[8:9], v[8:9], 0, s[46:47]
	global_load_lds_dwordx4 v[8:9], off
	s_waitcnt vmcnt(8)
	s_waitcnt lgkmcnt(0)
	s_barrier
	v_mfma_f32_16x16x128_f8f6f4 v[60:63], v[0:7], v[32:39], v[60:63]
	v_mfma_f32_16x16x128_f8f6f4 v[56:59], v[16:23], v[32:39], v[56:59]
	v_mfma_f32_16x16x128_f8f6f4 v[44:47], v[0:7], v[152:159], v[194:197]
	v_mfma_f32_16x16x128_f8f6f4 v[40:43], v[16:23], v[152:159], v[198:201]
	v_mfma_f32_16x16x128_f8f6f4 v[28:31], v[0:7], v[160:167], v[210:213]
	v_mfma_f32_16x16x128_f8f6f4 v[24:27], v[16:23], v[160:167], v[214:217]
	v_mfma_f32_16x16x128_f8f6f4 v[12:15], v[0:7], v[168:175], v[218:221]
	v_mfma_f32_16x16x128_f8f6f4 v[8:11], v[16:23], v[168:175], v[222:225]
	v_mfma_f32_16x16x128_f8f6f4 v[52:55], v[128:135], v[32:39], v[52:55]
	v_mfma_f32_16x16x128_f8f6f4 v[48:51], v[136:143], v[32:39], v[48:51]
	v_mfma_f32_16x16x128_f8f6f4 v[36:39], v[128:135], v[152:159], v[228:231]
	v_mfma_f32_16x16x128_f8f6f4 v[32:35], v[136:143], v[152:159], v[232:235]
	v_mfma_f32_16x16x128_f8f6f4 v[20:23], v[128:135], v[160:167], v[236:239]
	v_mfma_f32_16x16x128_f8f6f4 v[16:19], v[136:143], v[160:167], v[240:243]
	v_mfma_f32_16x16x128_f8f6f4 v[4:7], v[128:135], v[168:175], v[244:247]
	v_mfma_f32_16x16x128_f8f6f4 v[0:3], v[136:143], v[168:175], v[248:251]
	s_barrier
	s_add_i32 s81, s81, 2
	s_add_u32 s28, s28, 0x100
	s_addc_u32 s29, s29, 0
	s_add_u32 s25, s25, 0x100
	s_addc_u32 s80, s80, 0
.LBB0_1114:
	ds_read_b128 v[128:131], v148
	ds_read_b128 v[136:139], v148 offset:2048
	ds_read_b128 v[132:135], v149
	ds_read_b128 v[140:143], v149 offset:2048
	ds_read_b128 v[152:155], v148 offset:16384
	ds_read_b128 v[160:163], v148 offset:18432
	ds_read_b128 v[156:159], v149 offset:16384
	ds_read_b128 v[164:167], v149 offset:18432
	s_add_u32 s30, s28, 0xfffe0080
	s_addc_u32 s31, s29, -1
	s_cmp_eq_u32 s81, 4
	s_cselect_b32 s31, s7, s31
	s_cselect_b32 s30, s21, s30
	s_cselect_b32 s35, s19, s80
	s_cselect_b32 s34, s18, s25
	v_mov_b32_e32 v144, v150
	ds_read_b128 v[168:171], v146
	ds_read_b128 v[176:179], v146 offset:2048
	ds_read_b128 v[172:175], v147
	ds_read_b128 v[180:183], v147 offset:2048
	ds_read_b128 v[194:197], v146 offset:4096
	ds_read_b128 v[228:231], v146 offset:6144
	ds_read_b128 v[198:201], v147 offset:4096
	ds_read_b128 v[232:235], v147 offset:6144
	s_add_i32 m0, s27, 0xc000
	s_nop 0
	global_load_lds_dwordx4 v144, s[28:29]
	v_mov_b32_e32 v144, v151
	s_add_i32 m0, s27, 0xe000
	s_nop 0
	global_load_lds_dwordx4 v144, s[28:29]
	s_waitcnt vmcnt(8)
	s_waitcnt lgkmcnt(0)
	s_barrier
	v_mfma_f32_16x16x128_f8f6f4 v[124:127], v[128:135], v[168:175], v[124:127]
	v_mfma_f32_16x16x128_f8f6f4 v[120:123], v[136:143], v[168:175], v[120:123]
	v_mfma_f32_16x16x128_f8f6f4 v[108:111], v[128:135], v[176:183], v[108:111]
	v_mfma_f32_16x16x128_f8f6f4 v[104:107], v[136:143], v[176:183], v[104:107]
	v_mfma_f32_16x16x128_f8f6f4 v[186:189], v[128:135], v[194:201], v[92:95]
	v_mfma_f32_16x16x128_f8f6f4 v[190:193], v[136:143], v[194:201], v[88:91]
	v_mfma_f32_16x16x128_f8f6f4 v[202:205], v[128:135], v[228:235], v[76:79]
	v_mfma_f32_16x16x128_f8f6f4 v[206:209], v[136:143], v[228:235], v[72:75]
	v_mfma_f32_16x16x128_f8f6f4 v[116:119], v[152:159], v[168:175], v[116:119]
	v_mfma_f32_16x16x128_f8f6f4 v[112:115], v[160:167], v[168:175], v[112:115]
	v_mfma_f32_16x16x128_f8f6f4 v[100:103], v[152:159], v[176:183], v[100:103]
	v_mfma_f32_16x16x128_f8f6f4 v[96:99], v[160:167], v[176:183], v[96:99]
	v_mfma_f32_16x16x128_f8f6f4 v[168:171], v[152:159], v[194:201], v[84:87]
	v_mfma_f32_16x16x128_f8f6f4 v[172:175], v[160:167], v[194:201], v[80:83]
	v_mfma_f32_16x16x128_f8f6f4 v[176:179], v[152:159], v[228:235], v[68:71]
	v_mfma_f32_16x16x128_f8f6f4 v[180:183], v[160:167], v[228:235], v[64:67]
	s_barrier
	v_mov_b32_e32 v144, v150
	s_mov_b32 m0, s43
	s_nop 2
	ds_read_b128 v[64:67], v146 offset:16384
	ds_read_b128 v[72:75], v146 offset:18432
	ds_read_b128 v[68:71], v147 offset:16384
	ds_read_b128 v[76:79], v147 offset:18432
	ds_read_b128 v[80:83], v146 offset:20480
	ds_read_b128 v[88:91], v146 offset:22528
	ds_read_b128 v[84:87], v147 offset:20480
	ds_read_b128 v[92:95], v147 offset:22528
	s_add_u32 s82, s34, 0x20000
	global_load_lds_dwordx4 v144, s[34:35]
	v_mov_b32_e32 v144, v151
	s_mov_b32 m0, s44
	s_addc_u32 s83, s35, 0
	global_load_lds_dwordx4 v144, s[34:35]
	v_mov_b32_e32 v144, v150
	s_mov_b32 m0, s49
	s_nop 0
	global_load_lds_dwordx4 v144, s[82:83]
	v_mov_b32_e32 v144, v151
	s_mov_b32 m0, s50
	s_nop 0
	global_load_lds_dwordx4 v144, s[82:83]
	v_mov_b32_e32 v144, v150
	s_mov_b32 m0, s27
	s_nop 0
	global_load_lds_dwordx4 v144, s[30:31]
	v_mov_b32_e32 v144, v151
	s_mov_b32 m0, s51
	s_nop 0
	global_load_lds_dwordx4 v144, s[30:31]
	s_waitcnt vmcnt(8)
	s_waitcnt lgkmcnt(0)
	s_barrier
	v_mfma_f32_16x16x128_f8f6f4 v[60:63], v[128:135], v[64:71], v[60:63]
	v_mfma_f32_16x16x128_f8f6f4 v[56:59], v[136:143], v[64:71], v[56:59]
	v_mfma_f32_16x16x128_f8f6f4 v[194:197], v[128:135], v[72:79], v[44:47]
	v_mfma_f32_16x16x128_f8f6f4 v[198:201], v[136:143], v[72:79], v[40:43]
	v_mfma_f32_16x16x128_f8f6f4 v[210:213], v[128:135], v[80:87], v[28:31]
	v_mfma_f32_16x16x128_f8f6f4 v[214:217], v[136:143], v[80:87], v[24:27]
	v_mfma_f32_16x16x128_f8f6f4 v[218:221], v[128:135], v[88:95], v[12:15]
	v_mfma_f32_16x16x128_f8f6f4 v[222:225], v[136:143], v[88:95], v[8:11]
	v_mfma_f32_16x16x128_f8f6f4 v[52:55], v[152:159], v[64:71], v[52:55]
	v_mfma_f32_16x16x128_f8f6f4 v[48:51], v[160:167], v[64:71], v[48:51]
	v_mfma_f32_16x16x128_f8f6f4 v[228:231], v[152:159], v[72:79], v[36:39]
	v_mfma_f32_16x16x128_f8f6f4 v[232:235], v[160:167], v[72:79], v[32:35]
	v_mfma_f32_16x16x128_f8f6f4 v[236:239], v[152:159], v[80:87], v[20:23]
	v_mfma_f32_16x16x128_f8f6f4 v[240:243], v[160:167], v[80:87], v[16:19]
	v_mfma_f32_16x16x128_f8f6f4 v[244:247], v[152:159], v[88:95], v[4:7]
	v_mfma_f32_16x16x128_f8f6f4 v[248:251], v[160:167], v[88:95], v[0:3]
	s_barrier
	s_nop 4
	ds_read_b128 v[0:3], v148 offset:32768
	ds_read_b128 v[16:19], v148 offset:34816
	ds_read_b128 v[4:7], v149 offset:32768
	ds_read_b128 v[20:23], v149 offset:34816
	ds_read_b128 v[128:131], v148 offset:49152
	ds_read_b128 v[136:139], v148 offset:51200
	ds_read_b128 v[132:135], v149 offset:49152
	ds_read_b128 v[140:143], v149 offset:51200
	s_add_u32 s82, s30, 0x20000
	v_mov_b32_e32 v64, v150
	s_mov_b32 m0, s54
	ds_read_b128 v[8:11], v146 offset:32768
	ds_read_b128 v[24:27], v146 offset:34816
	ds_read_b128 v[12:15], v147 offset:32768
	ds_read_b128 v[28:31], v147 offset:34816
	ds_read_b128 v[32:35], v146 offset:36864
	ds_read_b128 v[40:43], v146 offset:38912
	ds_read_b128 v[36:39], v147 offset:36864
	ds_read_b128 v[44:47], v147 offset:38912
	s_addc_u32 s83, s31, 0
	s_nop 0
	global_load_lds_dwordx4 v64, s[82:83]
	v_mov_b32_e32 v64, v151
	s_mov_b32 m0, s55
	s_nop 0
	global_load_lds_dwordx4 v64, s[82:83]
	s_waitcnt vmcnt(8)
	s_waitcnt lgkmcnt(0)
	s_barrier
	v_mfma_f32_16x16x128_f8f6f4 v[124:127], v[0:7], v[8:15], v[124:127]
	v_mfma_f32_16x16x128_f8f6f4 v[120:123], v[16:23], v[8:15], v[120:123]
	v_mfma_f32_16x16x128_f8f6f4 v[108:111], v[0:7], v[24:31], v[108:111]
	v_mfma_f32_16x16x128_f8f6f4 v[104:107], v[16:23], v[24:31], v[104:107]
	v_mfma_f32_16x16x128_f8f6f4 v[92:95], v[0:7], v[32:39], v[186:189]
	v_mfma_f32_16x16x128_f8f6f4 v[88:91], v[16:23], v[32:39], v[190:193]
	v_mfma_f32_16x16x128_f8f6f4 v[76:79], v[0:7], v[40:47], v[202:205]
	v_mfma_f32_16x16x128_f8f6f4 v[72:75], v[16:23], v[40:47], v[206:209]
	v_mfma_f32_16x16x128_f8f6f4 v[116:119], v[128:135], v[8:15], v[116:119]
	v_mfma_f32_16x16x128_f8f6f4 v[112:115], v[136:143], v[8:15], v[112:115]
	v_mfma_f32_16x16x128_f8f6f4 v[100:103], v[128:135], v[24:31], v[100:103]
	v_mfma_f32_16x16x128_f8f6f4 v[96:99], v[136:143], v[24:31], v[96:99]
	v_mfma_f32_16x16x128_f8f6f4 v[84:87], v[128:135], v[32:39], v[168:171]
	v_mfma_f32_16x16x128_f8f6f4 v[80:83], v[136:143], v[32:39], v[172:175]
	v_mfma_f32_16x16x128_f8f6f4 v[68:71], v[128:135], v[40:47], v[176:179]
	v_mfma_f32_16x16x128_f8f6f4 v[64:67], v[136:143], v[40:47], v[180:183]
	s_barrier
	v_mov_b32_e32 v184, v150
	ds_read_b128 v[32:35], v146 offset:49152
	ds_read_b128 v[152:155], v146 offset:51200
	ds_read_b128 v[36:39], v147 offset:49152
	ds_read_b128 v[156:159], v147 offset:51200
	ds_read_b128 v[160:163], v146 offset:53248
	ds_read_b128 v[168:171], v146 offset:55296
	ds_read_b128 v[164:167], v147 offset:53248
	ds_read_b128 v[172:175], v147 offset:55296
	s_mov_b32 m0, s56
	v_lshl_add_u64 v[8:9], s[34:35], 0, v[184:185]
	v_lshl_add_u64 v[8:9], v[8:9], 0, s[46:47]
	v_mov_b32_e32 v184, v151
	global_load_lds_dwordx4 v[8:9], off
	s_mov_b32 m0, s57
	v_lshl_add_u64 v[8:9], s[34:35], 0, v[184:185]
	v_lshl_add_u64 v[8:9], v[8:9], 0, s[46:47]
	global_load_lds_dwordx4 v[8:9], off
	s_add_u32 s34, s34, 0x20080
	v_mov_b32_e32 v8, v150
	s_addc_u32 s35, s35, 0
	s_mov_b32 m0, s65
	v_mov_b32_e32 v184, v150
	global_load_lds_dwordx4 v8, s[34:35]
	v_mov_b32_e32 v8, v151
	s_mov_b32 m0, s66
	s_nop 0
	global_load_lds_dwordx4 v8, s[34:35]
	s_mov_b32 m0, s59
	v_lshl_add_u64 v[8:9], s[30:31], 0, v[184:185]
	v_lshl_add_u64 v[8:9], v[8:9], 0, s[46:47]
	v_mov_b32_e32 v184, v151
	global_load_lds_dwordx4 v[8:9], off
	s_mov_b32 m0, s64
	v_lshl_add_u64 v[8:9], s[30:31], 0, v[184:185]
	v_lshl_add_u64 v[8:9], v[8:9], 0, s[46:47]
	global_load_lds_dwordx4 v[8:9], off
	s_waitcnt vmcnt(8)
	s_waitcnt lgkmcnt(0)
	s_barrier
	v_mfma_f32_16x16x128_f8f6f4 v[60:63], v[0:7], v[32:39], v[60:63]
	v_mfma_f32_16x16x128_f8f6f4 v[56:59], v[16:23], v[32:39], v[56:59]
	v_mfma_f32_16x16x128_f8f6f4 v[44:47], v[0:7], v[152:159], v[194:197]
	v_mfma_f32_16x16x128_f8f6f4 v[40:43], v[16:23], v[152:159], v[198:201]
	v_mfma_f32_16x16x128_f8f6f4 v[28:31], v[0:7], v[160:167], v[210:213]
	v_mfma_f32_16x16x128_f8f6f4 v[24:27], v[16:23], v[160:167], v[214:217]
	v_mfma_f32_16x16x128_f8f6f4 v[12:15], v[0:7], v[168:175], v[218:221]
	v_mfma_f32_16x16x128_f8f6f4 v[8:11], v[16:23], v[168:175], v[222:225]
	v_mfma_f32_16x16x128_f8f6f4 v[52:55], v[128:135], v[32:39], v[52:55]
	v_mfma_f32_16x16x128_f8f6f4 v[48:51], v[136:143], v[32:39], v[48:51]
	v_mfma_f32_16x16x128_f8f6f4 v[36:39], v[128:135], v[152:159], v[228:231]
	v_mfma_f32_16x16x128_f8f6f4 v[32:35], v[136:143], v[152:159], v[232:235]
	v_mfma_f32_16x16x128_f8f6f4 v[20:23], v[128:135], v[160:167], v[236:239]
	v_mfma_f32_16x16x128_f8f6f4 v[16:19], v[136:143], v[160:167], v[240:243]
	v_mfma_f32_16x16x128_f8f6f4 v[4:7], v[128:135], v[168:175], v[244:247]
	v_mfma_f32_16x16x128_f8f6f4 v[0:3], v[136:143], v[168:175], v[248:251]
	s_barrier
	s_add_i32 s81, s81, 2
	s_add_u32 s28, s28, 0x100
	s_addc_u32 s29, s29, 0
	s_add_u32 s25, s25, 0x100
	s_addc_u32 s80, s80, 0
	s_cmp_gt_u32 s81, 5
	s_cbranch_scc0 .LBB0_1114
	s_and_b64 vcc, exec, s[10:11]
	s_mov_b32 s21, s20
	s_mov_b32 s28, s24
	s_mov_b64 s[10:11], 0
	s_cbranch_vccz .LBB0_1122
	s_add_i32 s7, s79, 2
	s_mul_i32 s10, s7, s67
	s_mul_hi_u32 s11, s7, s0
	s_add_i32 s11, s11, s10
	s_mul_i32 s7, s7, s0
	s_add_u32 s30, s7, s1
	s_addc_u32 s31, s11, s68
	v_mov_b64_e32 v[128:129], s[4:5]
	v_cmp_ge_i64_e32 vcc, s[30:31], v[128:129]
	s_mov_b64 s[10:11], 0
	s_mov_b32 s28, s24
	s_mov_b32 s21, s20
	s_cbranch_vccnz .LBB0_1122
	s_ashr_i32 s7, s30, 31
	s_lshr_b32 s7, s7, 29
	s_add_i32 s7, s30, s7
	s_and_b32 s10, s7, -8
	s_sub_i32 s21, s30, s10
	s_cmp_ge_i32 s21, s72
	s_mov_b64 s[10:11], -1
	s_cbranch_scc0 .LBB0_1119
	s_sub_i32 s10, s21, s72
	s_mul_i32 s10, s10, s70
	s_mul_i32 s11, s73, s72
	s_add_i32 s25, s10, s11
	s_mov_b64 s[10:11], 0
